# strategy 9 loop-edge edit: the GEMM K-loops' counter/pointer/exit-test SALU block moved in front of the loop-back barrier (5 loops); on top of m19
# baseline (speedup 1.0000x reference)
; #define PG8_STAGE(bufoff, gbase, voff) do { _Pragma("unroll") for (int _i = 0; _i < 2; ++_i) \
;         __builtin_amdgcn_global_load_lds((const unsigned*)((const char*)(gbase) + (voff)[_i]), (LAS unsigned*)(lds + (bufoff) + ldsw + _i * 8192), 16, 0, 0); } while (0)
; #define PG8_LDA(dst, b, h) do { if constexpr (F8) { _Pragma("unroll") for (int m = 0; m < 4; ++m) dst##8[m] = PG8_LD8(lds + PG8_SA(b, h) + aoff + m * 2048); } else { \
;         _Pragma("unroll") for (int m = 0; m < 4; ++m) _Pragma("unroll") for (int k = 0; k < 2; ++k) dst[m][k] = *(const LAS bf16x8*)(lds + PG8_SA(b, h) + aoff + m * 2048 + k * 1024); } } while (0)
; #define PG8_LDB(dst, b, h) do { if constexpr (F8) { _Pragma("unroll") for (int n = 0; n < 2; ++n) dst##8[n] = PG8_LD8(lds + PG8_SB(b, h) + boff + n * 2048); } else { \
;         _Pragma("unroll") for (int n = 0; n < 2; ++n) _Pragma("unroll") for (int k = 0; k < 2; ++k) dst[n][k] = *(const LAS bf16x8*)(lds + PG8_SB(b, h) + boff + n * 2048 + k * 1024); } } while (0)
; #define PG8_WAIT_L(n) asm volatile("s_waitcnt lgkmcnt(" #n ")" ::: "memory")
; #define PG8_BAR __builtin_amdgcn_s_barrier()
; template <class Epi, class Sched, bool F8 = false>
; DI void gemm_phase(LAS unsigned char* lds, const int K, const Sched& S, const Epi& E) {
;     ...
;         for (int t = 0; t < nt; t += 2) {
;             const bool last = (t == nt - 2); const int sxe = (t == 0) ? sx : 0;
;             const char* a1 = cA + (size_t)(t + 1) * kstep;
;             const char* a2 = last ? nA : cA + (size_t)(t + 2) * kstep; const char* b2 = last ? nB : cB + (size_t)(t + 2) * kstep;
;             const char* a3 = a2 + kstep; const char* b3 = b2 + kstep;
;             PG8_LDB(B0, 0, 0); PG8_LDB(B1, 0, 1); PG8_SCHED; PG8_LDA(At, 0, 0); PG8_STAGE(PG8_SA(1, 1), a1, oA[1]);
;             if (last && has_next) S.a_off(nxt, tid, oA);
;             PG8_WAIT_VX(sxe); PG8_WAIT_L(0); PG8_BAR; if (F8 && t == 0) { PG8_MMA0(0, 0, At, B0); PG8_MMA0(0, 1, At, B1); } else { PG8_MMA(0, 0, At, B0); PG8_MMA(0, 1, At, B1); } PG8_BAR; PG8_SCHED;
;             PG8_LDA(At, 0, 1); PG8_STAGE(PG8_SB(0, 0), b2, voffB); PG8_STAGE(PG8_SB(0, 1), b2 + hstep, voffB); PG8_STAGE(PG8_SA(0, 0), a2, oA[0]);
;             PG8_WAIT_VX(sxe); PG8_WAIT_L(0); PG8_BAR; if (F8 && t == 0) { PG8_MMA0(1, 0, At, B0); PG8_MMA0(1, 1, At, B1); } else { PG8_MMA(1, 0, At, B0); PG8_MMA(1, 1, At, B1); } PG8_BAR; PG8_SCHED;
.LBB0_276:
	ds_read_b128 v[6:9], v190
	ds_read_b128 v[10:13], v190 offset:1024
	ds_read_b128 v[22:25], v190 offset:2048
	ds_read_b128 v[26:29], v190 offset:3072
	ds_read_b128 v[30:33], v191
	ds_read_b128 v[34:37], v191 offset:1024
	ds_read_b128 v[180:183], v191 offset:2048
	ds_read_b128 v[184:187], v191 offset:3072
	s_add_u32 s9, s30, 0x200
	s_addc_u32 s10, s31, 0
	s_cmp_eq_u32 s8, 4
	s_cselect_b32 vcc_hi, s4, s10
	s_cselect_b32 vcc_lo, s5, s9
	s_cselect_b32 s67, s17, s7
	s_cselect_b32 s66, s43, s6
	s_mov_b32 m0, s47
	v_lshl_add_u64 v[220:221], s[30:31], 0, v[178:179]
	ds_read_b128 v[14:17], v189
	ds_read_b128 v[18:21], v189 offset:1024
	ds_read_b128 v[194:197], v189 offset:2048
	ds_read_b128 v[198:201], v189 offset:3072
	ds_read_b128 v[212:215], v189 offset:4096
	ds_read_b128 v[216:219], v189 offset:5120
	ds_read_b128 v[236:239], v189 offset:6144
	ds_read_b128 v[240:243], v189 offset:7168
	global_load_lds_dwordx4 v[220:221], off
	v_lshl_add_u64 v[220:221], s[30:31], 0, v[176:177]
	s_mov_b32 m0, s56
	s_nop 0
	global_load_lds_dwordx4 v[220:221], off
	s_waitcnt vmcnt(8)
	s_waitcnt lgkmcnt(0)
	s_barrier
	s_setprio 1
	s_waitcnt lgkmcnt(0)
	v_mfma_f32_16x16x128_f8f6f4 v[158:161], v[6:13], v[14:21], v[158:161]
	v_mfma_f32_16x16x128_f8f6f4 v[150:153], v[22:29], v[14:21], v[150:153]
	v_mfma_f32_16x16x128_f8f6f4 v[142:145], v[6:13], v[194:201], v[142:145]
	v_mfma_f32_16x16x128_f8f6f4 v[134:137], v[22:29], v[194:201], v[134:137]
	v_mfma_f32_16x16x128_f8f6f4 v[126:129], v[6:13], v[212:219], v[126:129]
	v_mfma_f32_16x16x128_f8f6f4 v[118:121], v[22:29], v[212:219], v[118:121]
	v_mfma_f32_16x16x128_f8f6f4 v[110:113], v[6:13], v[236:243], v[110:113]
	v_mfma_f32_16x16x128_f8f6f4 v[102:105], v[22:29], v[236:243], v[102:105]
	s_setprio 0
	s_setprio 1
	v_mfma_f32_16x16x128_f8f6f4 v[162:165], v[30:37], v[14:21], v[162:165]
	v_mfma_f32_16x16x128_f8f6f4 v[154:157], v[180:187], v[14:21], v[154:157]
	v_mfma_f32_16x16x128_f8f6f4 v[146:149], v[30:37], v[194:201], v[146:149]
	v_mfma_f32_16x16x128_f8f6f4 v[138:141], v[180:187], v[194:201], v[138:141]
	v_mfma_f32_16x16x128_f8f6f4 v[130:133], v[30:37], v[212:219], v[130:133]
	v_mfma_f32_16x16x128_f8f6f4 v[122:125], v[180:187], v[212:219], v[122:125]
	v_mfma_f32_16x16x128_f8f6f4 v[114:117], v[30:37], v[236:243], v[114:117]
	v_mfma_f32_16x16x128_f8f6f4 v[106:109], v[180:187], v[236:243], v[106:109]
	s_setprio 0
	s_barrier
	s_mov_b32 m0, s78
	v_lshl_add_u64 v[14:15], s[66:67], 0, v[2:3]
	s_add_u32 s10, s66, 0x20000
	ds_read_b128 v[194:197], v189 offset:16384
	ds_read_b128 v[198:201], v189 offset:17408
	ds_read_b128 v[212:215], v189 offset:18432
	ds_read_b128 v[216:219], v189 offset:19456
	ds_read_b128 v[236:239], v189 offset:20480
	ds_read_b128 v[240:243], v189 offset:21504
	ds_read_b128 v[244:247], v189 offset:22528
	ds_read_b128 v[248:251], v189 offset:23552
	global_load_lds_dwordx4 v[14:15], off
	v_lshl_add_u64 v[16:17], s[66:67], 0, v[166:167]
	s_mov_b32 m0, s79
	s_addc_u32 s11, s67, 0
	global_load_lds_dwordx4 v[16:17], off
	v_lshl_add_u64 v[18:19], s[10:11], 0, v[2:3]
	s_mov_b32 m0, s81
	v_lshl_add_u64 v[20:21], vcc, 0, v[172:173]
	global_load_lds_dwordx4 v[18:19], off
	v_lshl_add_u64 v[18:19], s[10:11], 0, v[166:167]
	s_mov_b32 m0, s82
	s_nop 0
	global_load_lds_dwordx4 v[18:19], off
	v_lshl_add_u64 v[18:19], vcc, 0, v[168:169]
	s_mov_b32 m0, s83
	s_nop 0
	global_load_lds_dwordx4 v[18:19], off
	s_mov_b32 m0, s84
	s_nop 0
	global_load_lds_dwordx4 v[20:21], off
	s_waitcnt vmcnt(8)
	s_waitcnt lgkmcnt(0)
	s_barrier
	s_setprio 1
	s_waitcnt lgkmcnt(0)
	v_mfma_f32_16x16x128_f8f6f4 v[94:97], v[6:13], v[194:201], v[94:97]
	v_mfma_f32_16x16x128_f8f6f4 v[86:89], v[22:29], v[194:201], v[86:89]
	v_mfma_f32_16x16x128_f8f6f4 v[78:81], v[6:13], v[212:219], v[78:81]
	v_mfma_f32_16x16x128_f8f6f4 v[70:73], v[22:29], v[212:219], v[70:73]
	v_mfma_f32_16x16x128_f8f6f4 v[62:65], v[6:13], v[236:243], v[62:65]
	v_mfma_f32_16x16x128_f8f6f4 v[54:57], v[22:29], v[236:243], v[54:57]
	v_mfma_f32_16x16x128_f8f6f4 v[46:49], v[6:13], v[244:251], v[46:49]
	v_mfma_f32_16x16x128_f8f6f4 v[38:41], v[22:29], v[244:251], v[38:41]
	s_setprio 0
	s_setprio 1
	v_mfma_f32_16x16x128_f8f6f4 v[98:101], v[30:37], v[194:201], v[98:101]
	v_mfma_f32_16x16x128_f8f6f4 v[90:93], v[180:187], v[194:201], v[90:93]
	v_mfma_f32_16x16x128_f8f6f4 v[82:85], v[30:37], v[212:219], v[82:85]
	v_mfma_f32_16x16x128_f8f6f4 v[74:77], v[180:187], v[212:219], v[74:77]
	v_mfma_f32_16x16x128_f8f6f4 v[66:69], v[30:37], v[236:243], v[66:69]
	v_mfma_f32_16x16x128_f8f6f4 v[58:61], v[180:187], v[236:243], v[58:61]
	v_mfma_f32_16x16x128_f8f6f4 v[50:53], v[30:37], v[244:251], v[50:53]
	v_mfma_f32_16x16x128_f8f6f4 v[42:45], v[180:187], v[244:251], v[42:45]
	s_setprio 0
	s_barrier
; #define PG8_STAGE(bufoff, gbase, voff) do { _Pragma("unroll") for (int _i = 0; _i < 2; ++_i) \
;         __builtin_amdgcn_global_load_lds((const unsigned*)((const char*)(gbase) + (voff)[_i]), (LAS unsigned*)(lds + (bufoff) + ldsw + _i * 8192), 16, 0, 0); } while (0)
; #define PG8_LDA(dst, b, h) do { if constexpr (F8) { _Pragma("unroll") for (int m = 0; m < 4; ++m) dst##8[m] = PG8_LD8(lds + PG8_SA(b, h) + aoff + m * 2048); } else { \
;         _Pragma("unroll") for (int m = 0; m < 4; ++m) _Pragma("unroll") for (int k = 0; k < 2; ++k) dst[m][k] = *(const LAS bf16x8*)(lds + PG8_SA(b, h) + aoff + m * 2048 + k * 1024); } } while (0)
; #define PG8_LDB(dst, b, h) do { if constexpr (F8) { _Pragma("unroll") for (int n = 0; n < 2; ++n) dst##8[n] = PG8_LD8(lds + PG8_SB(b, h) + boff + n * 2048); } else { \
;         _Pragma("unroll") for (int n = 0; n < 2; ++n) _Pragma("unroll") for (int k = 0; k < 2; ++k) dst[n][k] = *(const LAS bf16x8*)(lds + PG8_SB(b, h) + boff + n * 2048 + k * 1024); } } while (0)
; #define PG8_WAIT_V(n) asm volatile("s_waitcnt vmcnt(" #n ")" ::: "memory")
; #define PG8_WAIT_L(n) asm volatile("s_waitcnt lgkmcnt(" #n ")" ::: "memory")
; #define PG8_BAR __builtin_amdgcn_s_barrier()
; #define PG8_SCHED __builtin_amdgcn_sched_barrier(0)
; template <class Epi, class Sched, bool F8 = false>
; DI void gemm_phase(LAS unsigned char* lds, const int K, const Sched& S, const Epi& E) {
;     ...
;         for (int t = 0; t < nt; t += 2) {
;             const bool last = (t == nt - 2); const int sxe = (t == 0) ? sx : 0;
;             const char* a1 = cA + (size_t)(t + 1) * kstep;
;             const char* a2 = last ? nA : cA + (size_t)(t + 2) * kstep; const char* b2 = last ? nB : cB + (size_t)(t + 2) * kstep;
;             const char* a3 = a2 + kstep; const char* b3 = b2 + kstep;
;     ...
;             PG8_LDB(B0, 1, 0); PG8_LDB(B1, 1, 1); PG8_SCHED; PG8_LDA(At, 1, 0); PG8_STAGE(PG8_SA(0, 1), a2, oA[1]);
;             PG8_WAIT_V(8); PG8_WAIT_L(0); PG8_BAR; PG8_MMA(0, 0, At, B0); PG8_MMA(0, 1, At, B1); PG8_BAR; PG8_SCHED;
;             PG8_LDA(At, 1, 1); PG8_STAGE(PG8_SB(1, 0), b3, voffB); PG8_STAGE(PG8_SB(1, 1), b3 + hstep, voffB); PG8_STAGE(PG8_SA(1, 0), a3, oA[0]);
;             PG8_WAIT_V(8); PG8_WAIT_L(0); PG8_BAR; PG8_MMA(1, 0, At, B0); PG8_MMA(1, 1, At, B1); PG8_BAR; PG8_SCHED;
	ds_read_b128 v[22:25], v192
	ds_read_b128 v[26:29], v192 offset:1024
	ds_read_b128 v[30:33], v192 offset:2048
	ds_read_b128 v[34:37], v192 offset:3072
	ds_read_b128 v[6:9], v193
	ds_read_b128 v[10:13], v193 offset:1024
	ds_read_b128 v[180:183], v193 offset:2048
	ds_read_b128 v[184:187], v193 offset:3072
	s_mov_b32 m0, s85
	v_lshl_add_u64 v[220:221], vcc, 0, v[170:171]
	ds_read_b128 v[194:197], v189 offset:32768
	ds_read_b128 v[198:201], v189 offset:33792
	ds_read_b128 v[212:215], v189 offset:34816
	ds_read_b128 v[216:219], v189 offset:35840
	ds_read_b128 v[236:239], v189 offset:36864
	ds_read_b128 v[240:243], v189 offset:37888
	ds_read_b128 v[244:247], v189 offset:38912
	ds_read_b128 v[248:251], v189 offset:39936
	global_load_lds_dwordx4 v[220:221], off
	v_lshl_add_u64 v[220:221], vcc, 0, v[174:175]
	s_mov_b32 m0, s86
	s_nop 0
	global_load_lds_dwordx4 v[220:221], off
	s_waitcnt vmcnt(8)
	s_waitcnt lgkmcnt(0)
	s_barrier
	s_setprio 1
	s_waitcnt lgkmcnt(0)
	v_mfma_f32_16x16x128_f8f6f4 v[158:161], v[22:29], v[194:201], v[158:161]
	v_mfma_f32_16x16x128_f8f6f4 v[150:153], v[30:37], v[194:201], v[150:153]
	v_mfma_f32_16x16x128_f8f6f4 v[142:145], v[22:29], v[212:219], v[142:145]
	v_mfma_f32_16x16x128_f8f6f4 v[134:137], v[30:37], v[212:219], v[134:137]
	v_mfma_f32_16x16x128_f8f6f4 v[126:129], v[22:29], v[236:243], v[126:129]
	v_mfma_f32_16x16x128_f8f6f4 v[118:121], v[30:37], v[236:243], v[118:121]
	v_mfma_f32_16x16x128_f8f6f4 v[110:113], v[22:29], v[244:251], v[110:113]
	v_mfma_f32_16x16x128_f8f6f4 v[102:105], v[30:37], v[244:251], v[102:105]
	s_setprio 0
	s_setprio 1
	v_mfma_f32_16x16x128_f8f6f4 v[162:165], v[6:13], v[194:201], v[162:165]
	v_mfma_f32_16x16x128_f8f6f4 v[154:157], v[180:187], v[194:201], v[154:157]
	v_mfma_f32_16x16x128_f8f6f4 v[146:149], v[6:13], v[212:219], v[146:149]
	v_mfma_f32_16x16x128_f8f6f4 v[138:141], v[180:187], v[212:219], v[138:141]
	v_mfma_f32_16x16x128_f8f6f4 v[130:133], v[6:13], v[236:243], v[130:133]
	v_mfma_f32_16x16x128_f8f6f4 v[122:125], v[180:187], v[236:243], v[122:125]
	v_mfma_f32_16x16x128_f8f6f4 v[114:117], v[6:13], v[244:251], v[114:117]
	v_mfma_f32_16x16x128_f8f6f4 v[106:109], v[180:187], v[244:251], v[106:109]
	s_setprio 0
	s_barrier
	s_mov_b32 m0, s89
	v_lshl_add_u64 v[14:15], v[14:15], 0, s[24:25]
	s_add_u32 s10, s66, 0x20080
	ds_read_b128 v[194:197], v189 offset:49152
	ds_read_b128 v[198:201], v189 offset:50176
	ds_read_b128 v[212:215], v189 offset:51200
	ds_read_b128 v[216:219], v189 offset:52224
	ds_read_b128 v[236:239], v189 offset:53248
	ds_read_b128 v[240:243], v189 offset:54272
	ds_read_b128 v[244:247], v189 offset:55296
	ds_read_b128 v[248:251], v189 offset:56320
	global_load_lds_dwordx4 v[14:15], off
	v_lshl_add_u64 v[14:15], v[16:17], 0, s[24:25]
	s_mov_b32 m0, s90
	s_addc_u32 s11, s67, 0
	global_load_lds_dwordx4 v[14:15], off
	v_lshl_add_u64 v[14:15], s[10:11], 0, v[2:3]
	s_mov_b32 m0, s94
	s_nop 0
	global_load_lds_dwordx4 v[14:15], off
	v_lshl_add_u64 v[14:15], s[10:11], 0, v[166:167]
	s_mov_b32 m0, s95
	s_nop 0
	global_load_lds_dwordx4 v[14:15], off
	v_lshl_add_u64 v[14:15], v[18:19], 0, s[24:25]
	s_mov_b32 m0, s91
	s_nop 0
	global_load_lds_dwordx4 v[14:15], off
	v_lshl_add_u64 v[14:15], v[20:21], 0, s[24:25]
	s_mov_b32 m0, s92
	s_nop 0
	global_load_lds_dwordx4 v[14:15], off
	s_waitcnt vmcnt(8)
	s_waitcnt lgkmcnt(0)
	s_barrier
	s_setprio 1
	s_waitcnt lgkmcnt(0)
	v_mfma_f32_16x16x128_f8f6f4 v[94:97], v[22:29], v[194:201], v[94:97]
	v_mfma_f32_16x16x128_f8f6f4 v[86:89], v[30:37], v[194:201], v[86:89]
	v_mfma_f32_16x16x128_f8f6f4 v[78:81], v[22:29], v[212:219], v[78:81]
	v_mfma_f32_16x16x128_f8f6f4 v[70:73], v[30:37], v[212:219], v[70:73]
	v_mfma_f32_16x16x128_f8f6f4 v[62:65], v[22:29], v[236:243], v[62:65]
	v_mfma_f32_16x16x128_f8f6f4 v[54:57], v[30:37], v[236:243], v[54:57]
	v_mfma_f32_16x16x128_f8f6f4 v[46:49], v[22:29], v[244:251], v[46:49]
	v_mfma_f32_16x16x128_f8f6f4 v[38:41], v[30:37], v[244:251], v[38:41]
	s_setprio 0
	s_setprio 1
	v_mfma_f32_16x16x128_f8f6f4 v[98:101], v[6:13], v[194:201], v[98:101]
	v_mfma_f32_16x16x128_f8f6f4 v[90:93], v[180:187], v[194:201], v[90:93]
	v_mfma_f32_16x16x128_f8f6f4 v[82:85], v[6:13], v[212:219], v[82:85]
	v_mfma_f32_16x16x128_f8f6f4 v[74:77], v[180:187], v[212:219], v[74:77]
	v_mfma_f32_16x16x128_f8f6f4 v[66:69], v[6:13], v[236:243], v[66:69]
	v_mfma_f32_16x16x128_f8f6f4 v[58:61], v[180:187], v[236:243], v[58:61]
	v_mfma_f32_16x16x128_f8f6f4 v[50:53], v[6:13], v[244:251], v[50:53]
	v_mfma_f32_16x16x128_f8f6f4 v[42:45], v[180:187], v[244:251], v[42:45]
	s_setprio 0
	s_add_i32 s8, s8, 2
	s_add_u32 s6, s6, 0x100
	s_addc_u32 s7, s7, 0
	s_add_u32 s30, s30, 0x100
	s_addc_u32 s31, s31, 0
	s_cmp_gt_u32 s8, 5
	s_barrier
	s_cbranch_scc0 .LBB0_276
	s_and_b64 vcc, exec, s[0:1]
	s_cbranch_vccz .LBB0_279
	s_barrier

; #define PG8_STAGE(bufoff, gbase, voff) do { _Pragma("unroll") for (int _i = 0; _i < 2; ++_i) \
;         __builtin_amdgcn_global_load_lds((const unsigned*)((const char*)(gbase) + (voff)[_i]), (LAS unsigned*)(lds + (bufoff) + ldsw + _i * 8192), 16, 0, 0); } while (0)
; #define PG8_LDA(dst, b, h) do { if constexpr (F8) { _Pragma("unroll") for (int m = 0; m < 4; ++m) dst##8[m] = PG8_LD8(lds + PG8_SA(b, h) + aoff + m * 2048); } else { \
;         _Pragma("unroll") for (int m = 0; m < 4; ++m) _Pragma("unroll") for (int k = 0; k < 2; ++k) dst[m][k] = *(const LAS bf16x8*)(lds + PG8_SA(b, h) + aoff + m * 2048 + k * 1024); } } while (0)
; #define PG8_LDB(dst, b, h) do { if constexpr (F8) { _Pragma("unroll") for (int n = 0; n < 2; ++n) dst##8[n] = PG8_LD8(lds + PG8_SB(b, h) + boff + n * 2048); } else { \
;         _Pragma("unroll") for (int n = 0; n < 2; ++n) _Pragma("unroll") for (int k = 0; k < 2; ++k) dst[n][k] = *(const LAS bf16x8*)(lds + PG8_SB(b, h) + boff + n * 2048 + k * 1024); } } while (0)
; #define PG8_WAIT_L(n) asm volatile("s_waitcnt lgkmcnt(" #n ")" ::: "memory")
; #define PG8_BAR __builtin_amdgcn_s_barrier()
; template <class Epi, class Sched, bool F8 = false>
; DI void gemm_phase(LAS unsigned char* lds, const int K, const Sched& S, const Epi& E) {
;     ...
;         for (int t = 0; t < nt; t += 2) {
;             const bool last = (t == nt - 2); const int sxe = (t == 0) ? sx : 0;
;             const char* a1 = cA + (size_t)(t + 1) * kstep;
;             const char* a2 = last ? nA : cA + (size_t)(t + 2) * kstep; const char* b2 = last ? nB : cB + (size_t)(t + 2) * kstep;
;             const char* a3 = a2 + kstep; const char* b3 = b2 + kstep;
;             PG8_LDB(B0, 0, 0); PG8_LDB(B1, 0, 1); PG8_SCHED; PG8_LDA(At, 0, 0); PG8_STAGE(PG8_SA(1, 1), a1, oA[1]);
;             if (last && has_next) S.a_off(nxt, tid, oA);
;             PG8_WAIT_VX(sxe); PG8_WAIT_L(0); PG8_BAR; if (F8 && t == 0) { PG8_MMA0(0, 0, At, B0); PG8_MMA0(0, 1, At, B1); } else { PG8_MMA(0, 0, At, B0); PG8_MMA(0, 1, At, B1); } PG8_BAR; PG8_SCHED;
;             PG8_LDA(At, 0, 1); PG8_STAGE(PG8_SB(0, 0), b2, voffB); PG8_STAGE(PG8_SB(0, 1), b2 + hstep, voffB); PG8_STAGE(PG8_SA(0, 0), a2, oA[0]);
;             PG8_WAIT_VX(sxe); PG8_WAIT_L(0); PG8_BAR; if (F8 && t == 0) { PG8_MMA0(1, 0, At, B0); PG8_MMA0(1, 1, At, B1); } else { PG8_MMA(1, 0, At, B0); PG8_MMA(1, 1, At, B1); } PG8_BAR; PG8_SCHED;
.LBB0_903:
	ds_read_b128 v[6:9], v188
	ds_read_b128 v[10:13], v188 offset:1024
	ds_read_b128 v[22:25], v188 offset:2048
	ds_read_b128 v[26:29], v188 offset:3072
	ds_read_b128 v[30:33], v189
	ds_read_b128 v[34:37], v189 offset:1024
	ds_read_b128 v[180:183], v189 offset:2048
	ds_read_b128 v[184:187], v189 offset:3072
	s_add_u32 s9, s56, 0x200
	s_addc_u32 s10, s57, 0
	s_cmp_eq_u32 s8, 4
	s_cselect_b32 s61, s49, s10
	s_cselect_b32 s60, s95, s9
	s_cselect_b32 s59, s47, s7
	s_cselect_b32 s58, s96, s6
	s_mov_b32 m0, s97
	v_lshl_add_u64 v[200:201], s[56:57], 0, v[178:179]
	ds_read_b128 v[14:17], v214
	ds_read_b128 v[18:21], v214 offset:1024
	ds_read_b128 v[192:195], v214 offset:2048
	ds_read_b128 v[196:199], v214 offset:3072
	ds_read_b128 v[226:229], v214 offset:4096
	ds_read_b128 v[230:233], v214 offset:5120
	ds_read_b128 v[236:239], v214 offset:6144
	ds_read_b128 v[240:243], v214 offset:7168
	global_load_lds_dwordx4 v[200:201], off
	v_lshl_add_u64 v[200:201], s[56:57], 0, v[176:177]
	s_mov_b32 m0, vcc_lo
	s_nop 0
	global_load_lds_dwordx4 v[200:201], off
	s_waitcnt vmcnt(8)
	s_waitcnt lgkmcnt(0)
	s_barrier
	s_setprio 1
	s_waitcnt lgkmcnt(0)
	v_mfma_f32_16x16x128_f8f6f4 v[162:165], v[6:13], v[14:21], v[162:165]
	v_mfma_f32_16x16x128_f8f6f4 v[158:161], v[22:29], v[14:21], v[158:161]
	v_mfma_f32_16x16x128_f8f6f4 v[146:149], v[6:13], v[192:199], v[146:149]
	v_mfma_f32_16x16x128_f8f6f4 v[142:145], v[22:29], v[192:199], v[142:145]
	v_mfma_f32_16x16x128_f8f6f4 v[130:133], v[6:13], v[226:233], v[130:133]
	v_mfma_f32_16x16x128_f8f6f4 v[126:129], v[22:29], v[226:233], v[126:129]
	v_mfma_f32_16x16x128_f8f6f4 v[114:117], v[6:13], v[236:243], v[114:117]
	v_mfma_f32_16x16x128_f8f6f4 v[110:113], v[22:29], v[236:243], v[110:113]
	s_setprio 0
	s_setprio 1
	v_mfma_f32_16x16x128_f8f6f4 v[154:157], v[30:37], v[14:21], v[154:157]
	v_mfma_f32_16x16x128_f8f6f4 v[150:153], v[180:187], v[14:21], v[150:153]
	v_mfma_f32_16x16x128_f8f6f4 v[138:141], v[30:37], v[192:199], v[138:141]
	v_mfma_f32_16x16x128_f8f6f4 v[134:137], v[180:187], v[192:199], v[134:137]
	v_mfma_f32_16x16x128_f8f6f4 v[122:125], v[30:37], v[226:233], v[122:125]
	v_mfma_f32_16x16x128_f8f6f4 v[118:121], v[180:187], v[226:233], v[118:121]
	v_mfma_f32_16x16x128_f8f6f4 v[98:101], v[30:37], v[236:243], v[98:101]
	v_mfma_f32_16x16x128_f8f6f4 v[94:97], v[180:187], v[236:243], v[94:97]
	s_setprio 0
	s_barrier
	s_mov_b32 m0, s68
	v_lshl_add_u64 v[14:15], s[58:59], 0, v[2:3]
	s_add_u32 s10, s58, 0x20000
	ds_read_b128 v[192:195], v214 offset:16384
	ds_read_b128 v[196:199], v214 offset:17408
	ds_read_b128 v[226:229], v214 offset:18432
	ds_read_b128 v[230:233], v214 offset:19456
	ds_read_b128 v[236:239], v214 offset:20480
	ds_read_b128 v[240:243], v214 offset:21504
	ds_read_b128 v[244:247], v214 offset:22528
	ds_read_b128 v[248:251], v214 offset:23552
	global_load_lds_dwordx4 v[14:15], off
	v_lshl_add_u64 v[16:17], s[58:59], 0, v[166:167]
	s_mov_b32 m0, s74
	s_addc_u32 s11, s59, 0
	global_load_lds_dwordx4 v[16:17], off
	v_lshl_add_u64 v[18:19], s[10:11], 0, v[2:3]
	s_mov_b32 m0, s76
	v_lshl_add_u64 v[20:21], s[60:61], 0, v[172:173]
	global_load_lds_dwordx4 v[18:19], off
	v_lshl_add_u64 v[18:19], s[10:11], 0, v[166:167]
	s_mov_b32 m0, s78
	s_nop 0
	global_load_lds_dwordx4 v[18:19], off
	v_lshl_add_u64 v[18:19], s[60:61], 0, v[168:169]
	s_mov_b32 m0, s79
	s_nop 0
	global_load_lds_dwordx4 v[18:19], off
	s_mov_b32 m0, s80
	s_nop 0
	global_load_lds_dwordx4 v[20:21], off
	s_waitcnt vmcnt(8)
	s_waitcnt lgkmcnt(0)
	s_barrier
	s_setprio 1
	s_waitcnt lgkmcnt(0)
	v_mfma_f32_16x16x128_f8f6f4 v[106:109], v[6:13], v[192:199], v[106:109]
	v_mfma_f32_16x16x128_f8f6f4 v[102:105], v[22:29], v[192:199], v[102:105]
	v_mfma_f32_16x16x128_f8f6f4 v[82:85], v[6:13], v[226:233], v[82:85]
	v_mfma_f32_16x16x128_f8f6f4 v[78:81], v[22:29], v[226:233], v[78:81]
	v_mfma_f32_16x16x128_f8f6f4 v[66:69], v[6:13], v[236:243], v[66:69]
	v_mfma_f32_16x16x128_f8f6f4 v[62:65], v[22:29], v[236:243], v[62:65]
	v_mfma_f32_16x16x128_f8f6f4 v[50:53], v[6:13], v[244:251], v[50:53]
	v_mfma_f32_16x16x128_f8f6f4 v[46:49], v[22:29], v[244:251], v[46:49]
	s_setprio 0
	s_setprio 1
	v_mfma_f32_16x16x128_f8f6f4 v[90:93], v[30:37], v[192:199], v[90:93]
	v_mfma_f32_16x16x128_f8f6f4 v[86:89], v[180:187], v[192:199], v[86:89]
	v_mfma_f32_16x16x128_f8f6f4 v[74:77], v[30:37], v[226:233], v[74:77]
	v_mfma_f32_16x16x128_f8f6f4 v[70:73], v[180:187], v[226:233], v[70:73]
	v_mfma_f32_16x16x128_f8f6f4 v[58:61], v[30:37], v[236:243], v[58:61]
	v_mfma_f32_16x16x128_f8f6f4 v[54:57], v[180:187], v[236:243], v[54:57]
	v_mfma_f32_16x16x128_f8f6f4 v[42:45], v[30:37], v[244:251], v[42:45]
	v_mfma_f32_16x16x128_f8f6f4 v[38:41], v[180:187], v[244:251], v[38:41]
	s_setprio 0
	s_barrier
; #define PG8_STAGE(bufoff, gbase, voff) do { _Pragma("unroll") for (int _i = 0; _i < 2; ++_i) \
;         __builtin_amdgcn_global_load_lds((const unsigned*)((const char*)(gbase) + (voff)[_i]), (LAS unsigned*)(lds + (bufoff) + ldsw + _i * 8192), 16, 0, 0); } while (0)
; #define PG8_LDA(dst, b, h) do { if constexpr (F8) { _Pragma("unroll") for (int m = 0; m < 4; ++m) dst##8[m] = PG8_LD8(lds + PG8_SA(b, h) + aoff + m * 2048); } else { \
;         _Pragma("unroll") for (int m = 0; m < 4; ++m) _Pragma("unroll") for (int k = 0; k < 2; ++k) dst[m][k] = *(const LAS bf16x8*)(lds + PG8_SA(b, h) + aoff + m * 2048 + k * 1024); } } while (0)
; #define PG8_LDB(dst, b, h) do { if constexpr (F8) { _Pragma("unroll") for (int n = 0; n < 2; ++n) dst##8[n] = PG8_LD8(lds + PG8_SB(b, h) + boff + n * 2048); } else { \
;         _Pragma("unroll") for (int n = 0; n < 2; ++n) _Pragma("unroll") for (int k = 0; k < 2; ++k) dst[n][k] = *(const LAS bf16x8*)(lds + PG8_SB(b, h) + boff + n * 2048 + k * 1024); } } while (0)
; #define PG8_WAIT_V(n) asm volatile("s_waitcnt vmcnt(" #n ")" ::: "memory")
; #define PG8_WAIT_L(n) asm volatile("s_waitcnt lgkmcnt(" #n ")" ::: "memory")
; #define PG8_BAR __builtin_amdgcn_s_barrier()
; #define PG8_SCHED __builtin_amdgcn_sched_barrier(0)
; template <class Epi, class Sched, bool F8 = false>
; DI void gemm_phase(LAS unsigned char* lds, const int K, const Sched& S, const Epi& E) {
;     ...
;             PG8_LDB(B0, 1, 0); PG8_LDB(B1, 1, 1); PG8_SCHED; PG8_LDA(At, 1, 0); PG8_STAGE(PG8_SA(0, 1), a2, oA[1]);
;             PG8_WAIT_V(8); PG8_WAIT_L(0); PG8_BAR; PG8_MMA(0, 0, At, B0); PG8_MMA(0, 1, At, B1); PG8_BAR; PG8_SCHED;
;             PG8_LDA(At, 1, 1); PG8_STAGE(PG8_SB(1, 0), b3, voffB); PG8_STAGE(PG8_SB(1, 1), b3 + hstep, voffB); PG8_STAGE(PG8_SA(1, 0), a3, oA[0]);
;             PG8_WAIT_V(8); PG8_WAIT_L(0); PG8_BAR; PG8_MMA(1, 0, At, B0); PG8_MMA(1, 1, At, B1); PG8_BAR; PG8_SCHED;
	ds_read_b128 v[22:25], v190
	ds_read_b128 v[26:29], v190 offset:1024
	ds_read_b128 v[30:33], v190 offset:2048
	ds_read_b128 v[34:37], v190 offset:3072
	ds_read_b128 v[6:9], v191
	ds_read_b128 v[10:13], v191 offset:1024
	ds_read_b128 v[180:183], v191 offset:2048
	ds_read_b128 v[184:187], v191 offset:3072
	s_mov_b32 m0, s81
	v_lshl_add_u64 v[200:201], s[60:61], 0, v[170:171]
	ds_read_b128 v[192:195], v214 offset:32768
	ds_read_b128 v[196:199], v214 offset:33792
	ds_read_b128 v[226:229], v214 offset:34816
	ds_read_b128 v[230:233], v214 offset:35840
	ds_read_b128 v[236:239], v214 offset:36864
	ds_read_b128 v[240:243], v214 offset:37888
	ds_read_b128 v[244:247], v214 offset:38912
	ds_read_b128 v[248:251], v214 offset:39936
	global_load_lds_dwordx4 v[200:201], off
	v_lshl_add_u64 v[200:201], s[60:61], 0, v[174:175]
	s_mov_b32 m0, s82
	s_nop 0
	global_load_lds_dwordx4 v[200:201], off
	s_waitcnt vmcnt(8)
	s_waitcnt lgkmcnt(0)
	s_barrier
	s_setprio 1
	s_waitcnt lgkmcnt(0)
	v_mfma_f32_16x16x128_f8f6f4 v[162:165], v[22:29], v[192:199], v[162:165]
	v_mfma_f32_16x16x128_f8f6f4 v[158:161], v[30:37], v[192:199], v[158:161]
	v_mfma_f32_16x16x128_f8f6f4 v[146:149], v[22:29], v[226:233], v[146:149]
	v_mfma_f32_16x16x128_f8f6f4 v[142:145], v[30:37], v[226:233], v[142:145]
	v_mfma_f32_16x16x128_f8f6f4 v[130:133], v[22:29], v[236:243], v[130:133]
	v_mfma_f32_16x16x128_f8f6f4 v[126:129], v[30:37], v[236:243], v[126:129]
	v_mfma_f32_16x16x128_f8f6f4 v[114:117], v[22:29], v[244:251], v[114:117]
	v_mfma_f32_16x16x128_f8f6f4 v[110:113], v[30:37], v[244:251], v[110:113]
	s_setprio 0
	s_setprio 1
	v_mfma_f32_16x16x128_f8f6f4 v[154:157], v[6:13], v[192:199], v[154:157]
	v_mfma_f32_16x16x128_f8f6f4 v[150:153], v[180:187], v[192:199], v[150:153]
	v_mfma_f32_16x16x128_f8f6f4 v[138:141], v[6:13], v[226:233], v[138:141]
	v_mfma_f32_16x16x128_f8f6f4 v[134:137], v[180:187], v[226:233], v[134:137]
	v_mfma_f32_16x16x128_f8f6f4 v[122:125], v[6:13], v[236:243], v[122:125]
	v_mfma_f32_16x16x128_f8f6f4 v[118:121], v[180:187], v[236:243], v[118:121]
	v_mfma_f32_16x16x128_f8f6f4 v[98:101], v[6:13], v[244:251], v[98:101]
	v_mfma_f32_16x16x128_f8f6f4 v[94:97], v[180:187], v[244:251], v[94:97]
	s_setprio 0
	s_barrier
	s_mov_b32 m0, s86
	v_lshl_add_u64 v[14:15], v[14:15], 0, s[24:25]
	s_add_u32 s10, s58, 0x20080
	ds_read_b128 v[192:195], v214 offset:49152
	ds_read_b128 v[196:199], v214 offset:50176
	ds_read_b128 v[226:229], v214 offset:51200
	ds_read_b128 v[230:233], v214 offset:52224
	ds_read_b128 v[236:239], v214 offset:53248
	ds_read_b128 v[240:243], v214 offset:54272
	ds_read_b128 v[244:247], v214 offset:55296
	ds_read_b128 v[248:251], v214 offset:56320
	global_load_lds_dwordx4 v[14:15], off
	v_lshl_add_u64 v[14:15], v[16:17], 0, s[24:25]
	s_mov_b32 m0, s87
	s_addc_u32 s11, s59, 0
	global_load_lds_dwordx4 v[14:15], off
	v_lshl_add_u64 v[14:15], s[10:11], 0, v[2:3]
	s_mov_b32 m0, s91
	s_nop 0
	global_load_lds_dwordx4 v[14:15], off
	v_lshl_add_u64 v[14:15], s[10:11], 0, v[166:167]
	s_mov_b32 m0, s92
	s_nop 0
	global_load_lds_dwordx4 v[14:15], off
	v_lshl_add_u64 v[14:15], v[18:19], 0, s[24:25]
	s_mov_b32 m0, s88
	s_nop 0
	global_load_lds_dwordx4 v[14:15], off
	v_lshl_add_u64 v[14:15], v[20:21], 0, s[24:25]
	s_mov_b32 m0, s89
	s_nop 0
	global_load_lds_dwordx4 v[14:15], off
	s_waitcnt vmcnt(8)
	s_waitcnt lgkmcnt(0)
	s_barrier
	s_setprio 1
	s_waitcnt lgkmcnt(0)
	v_mfma_f32_16x16x128_f8f6f4 v[106:109], v[22:29], v[192:199], v[106:109]
	v_mfma_f32_16x16x128_f8f6f4 v[102:105], v[30:37], v[192:199], v[102:105]
	v_mfma_f32_16x16x128_f8f6f4 v[82:85], v[22:29], v[226:233], v[82:85]
	v_mfma_f32_16x16x128_f8f6f4 v[78:81], v[30:37], v[226:233], v[78:81]
	v_mfma_f32_16x16x128_f8f6f4 v[66:69], v[22:29], v[236:243], v[66:69]
	v_mfma_f32_16x16x128_f8f6f4 v[62:65], v[30:37], v[236:243], v[62:65]
	v_mfma_f32_16x16x128_f8f6f4 v[50:53], v[22:29], v[244:251], v[50:53]
	v_mfma_f32_16x16x128_f8f6f4 v[46:49], v[30:37], v[244:251], v[46:49]
	s_setprio 0
	s_setprio 1
	v_mfma_f32_16x16x128_f8f6f4 v[90:93], v[6:13], v[192:199], v[90:93]
	v_mfma_f32_16x16x128_f8f6f4 v[86:89], v[180:187], v[192:199], v[86:89]
	v_mfma_f32_16x16x128_f8f6f4 v[74:77], v[6:13], v[226:233], v[74:77]
	v_mfma_f32_16x16x128_f8f6f4 v[70:73], v[180:187], v[226:233], v[70:73]
	v_mfma_f32_16x16x128_f8f6f4 v[58:61], v[6:13], v[236:243], v[58:61]
	v_mfma_f32_16x16x128_f8f6f4 v[54:57], v[180:187], v[236:243], v[54:57]
	v_mfma_f32_16x16x128_f8f6f4 v[42:45], v[6:13], v[244:251], v[42:45]
	v_mfma_f32_16x16x128_f8f6f4 v[38:41], v[180:187], v[244:251], v[38:41]
	s_setprio 0
	s_add_i32 s8, s8, 2
	s_add_u32 s6, s6, 0x100
	s_addc_u32 s7, s7, 0
	s_add_u32 s56, s56, 0x100
	s_addc_u32 s57, s57, 0
	s_cmp_gt_u32 s8, 5
	s_barrier
	s_cbranch_scc0 .LBB0_903
	v_readlane_b32 s96, v254, 24
	s_and_b64 vcc, exec, s[44:45]
	v_readlane_b32 s97, v254, 25
	s_movk_i32 s95, 0x90
	v_mov_b32_e32 v248, v203
	v_mov_b64_e32 v[250:251], v[216:217]
	s_cbranch_vccz .LBB0_906
	s_barrier

; #define PG8_STAGE(bufoff, gbase, voff) do { _Pragma("unroll") for (int _i = 0; _i < 2; ++_i) \
;         __builtin_amdgcn_global_load_lds((const unsigned*)((const char*)(gbase) + (voff)[_i]), (LAS unsigned*)(lds + (bufoff) + ldsw + _i * 8192), 16, 0, 0); } while (0)
; #define PG8_LDA(dst, b, h) do { if constexpr (F8) { _Pragma("unroll") for (int m = 0; m < 4; ++m) dst##8[m] = PG8_LD8(lds + PG8_SA(b, h) + aoff + m * 2048); } else { \
;         _Pragma("unroll") for (int m = 0; m < 4; ++m) _Pragma("unroll") for (int k = 0; k < 2; ++k) dst[m][k] = *(const LAS bf16x8*)(lds + PG8_SA(b, h) + aoff + m * 2048 + k * 1024); } } while (0)
; #define PG8_LDB(dst, b, h) do { if constexpr (F8) { _Pragma("unroll") for (int n = 0; n < 2; ++n) dst##8[n] = PG8_LD8(lds + PG8_SB(b, h) + boff + n * 2048); } else { \
;         _Pragma("unroll") for (int n = 0; n < 2; ++n) _Pragma("unroll") for (int k = 0; k < 2; ++k) dst[n][k] = *(const LAS bf16x8*)(lds + PG8_SB(b, h) + boff + n * 2048 + k * 1024); } } while (0)
; #define PG8_WAIT_L(n) asm volatile("s_waitcnt lgkmcnt(" #n ")" ::: "memory")
; #define PG8_BAR __builtin_amdgcn_s_barrier()
; template <class Epi, class Sched, bool F8 = false>
; DI void gemm_phase(LAS unsigned char* lds, const int K, const Sched& S, const Epi& E) {
;     ...
;         for (int t = 0; t < nt; t += 2) {
;             const bool last = (t == nt - 2); const int sxe = (t == 0) ? sx : 0;
;             const char* a1 = cA + (size_t)(t + 1) * kstep;
;             const char* a2 = last ? nA : cA + (size_t)(t + 2) * kstep; const char* b2 = last ? nB : cB + (size_t)(t + 2) * kstep;
;             const char* a3 = a2 + kstep; const char* b3 = b2 + kstep;
;             PG8_LDB(B0, 0, 0); PG8_LDB(B1, 0, 1); PG8_SCHED; PG8_LDA(At, 0, 0); PG8_STAGE(PG8_SA(1, 1), a1, oA[1]);
;             if (last && has_next) S.a_off(nxt, tid, oA);
;             PG8_WAIT_VX(sxe); PG8_WAIT_L(0); PG8_BAR; if (F8 && t == 0) { PG8_MMA0(0, 0, At, B0); PG8_MMA0(0, 1, At, B1); } else { PG8_MMA(0, 0, At, B0); PG8_MMA(0, 1, At, B1); } PG8_BAR; PG8_SCHED;
;             PG8_LDA(At, 0, 1); PG8_STAGE(PG8_SB(0, 0), b2, voffB); PG8_STAGE(PG8_SB(0, 1), b2 + hstep, voffB); PG8_STAGE(PG8_SA(0, 0), a2, oA[0]);
;             PG8_WAIT_VX(sxe); PG8_WAIT_L(0); PG8_BAR; if (F8 && t == 0) { PG8_MMA0(1, 0, At, B0); PG8_MMA0(1, 1, At, B1); } else { PG8_MMA(1, 0, At, B0); PG8_MMA(1, 1, At, B1); } PG8_BAR; PG8_SCHED;
.LBB0_1043:
	ds_read_b128 v[6:9], v190
	ds_read_b128 v[10:13], v190 offset:1024
	ds_read_b128 v[22:25], v190 offset:2048
	ds_read_b128 v[26:29], v190 offset:3072
	ds_read_b128 v[30:33], v191
	ds_read_b128 v[34:37], v191 offset:1024
	ds_read_b128 v[180:183], v191 offset:2048
	ds_read_b128 v[184:187], v191 offset:3072
	s_add_u32 s10, s58, 0x200
	s_addc_u32 s11, s59, 0
	s_cmp_eq_u32 s9, 4
	s_cselect_b32 s63, s17, s11
	s_cselect_b32 s62, s53, s10
	s_cselect_b32 s61, s51, s8
	s_cselect_b32 s60, vcc_lo, s7
	s_mov_b32 m0, vcc_hi
	v_lshl_add_u64 v[220:221], s[58:59], 0, v[178:179]
	ds_read_b128 v[14:17], v189
	ds_read_b128 v[18:21], v189 offset:1024
	ds_read_b128 v[194:197], v189 offset:2048
	ds_read_b128 v[198:201], v189 offset:3072
	ds_read_b128 v[212:215], v189 offset:4096
	ds_read_b128 v[216:219], v189 offset:5120
	ds_read_b128 v[226:229], v189 offset:6144
	ds_read_b128 v[230:233], v189 offset:7168
	global_load_lds_dwordx4 v[220:221], off
	v_lshl_add_u64 v[220:221], s[58:59], 0, v[176:177]
	s_mov_b32 m0, s83
	s_nop 0
	global_load_lds_dwordx4 v[220:221], off
	s_waitcnt vmcnt(8)
	s_waitcnt lgkmcnt(0)
	s_barrier
	s_setprio 1
	s_waitcnt lgkmcnt(0)
	v_mfma_f32_16x16x128_f8f6f4 v[162:165], v[6:13], v[14:21], v[162:165]
	v_mfma_f32_16x16x128_f8f6f4 v[158:161], v[22:29], v[14:21], v[158:161]
	v_mfma_f32_16x16x128_f8f6f4 v[146:149], v[6:13], v[194:201], v[146:149]
	v_mfma_f32_16x16x128_f8f6f4 v[142:145], v[22:29], v[194:201], v[142:145]
	v_mfma_f32_16x16x128_f8f6f4 v[130:133], v[6:13], v[212:219], v[130:133]
	v_mfma_f32_16x16x128_f8f6f4 v[126:129], v[22:29], v[212:219], v[126:129]
	v_mfma_f32_16x16x128_f8f6f4 v[114:117], v[6:13], v[226:233], v[114:117]
	v_mfma_f32_16x16x128_f8f6f4 v[110:113], v[22:29], v[226:233], v[110:113]
	s_setprio 0
	s_setprio 1
	v_mfma_f32_16x16x128_f8f6f4 v[154:157], v[30:37], v[14:21], v[154:157]
	v_mfma_f32_16x16x128_f8f6f4 v[150:153], v[180:187], v[14:21], v[150:153]
	v_mfma_f32_16x16x128_f8f6f4 v[138:141], v[30:37], v[194:201], v[138:141]
	v_mfma_f32_16x16x128_f8f6f4 v[134:137], v[180:187], v[194:201], v[134:137]
	v_mfma_f32_16x16x128_f8f6f4 v[122:125], v[30:37], v[212:219], v[122:125]
	v_mfma_f32_16x16x128_f8f6f4 v[118:121], v[180:187], v[212:219], v[118:121]
	v_mfma_f32_16x16x128_f8f6f4 v[98:101], v[30:37], v[226:233], v[98:101]
	v_mfma_f32_16x16x128_f8f6f4 v[90:93], v[180:187], v[226:233], v[90:93]
	s_setprio 0
	s_barrier
	s_mov_b32 m0, s78
	v_lshl_add_u64 v[14:15], s[60:61], 0, v[2:3]
	s_add_u32 s10, s60, 0x20000
	ds_read_b128 v[194:197], v189 offset:16384
	ds_read_b128 v[198:201], v189 offset:17408
	ds_read_b128 v[212:215], v189 offset:18432
	ds_read_b128 v[216:219], v189 offset:19456
	ds_read_b128 v[226:229], v189 offset:20480
	ds_read_b128 v[230:233], v189 offset:21504
	ds_read_b128 v[236:239], v189 offset:22528
	ds_read_b128 v[240:243], v189 offset:23552
	global_load_lds_dwordx4 v[14:15], off
	v_lshl_add_u64 v[16:17], s[60:61], 0, v[166:167]
	s_mov_b32 m0, s79
	s_addc_u32 s11, s61, 0
	global_load_lds_dwordx4 v[16:17], off
	v_lshl_add_u64 v[18:19], s[10:11], 0, v[2:3]
	s_mov_b32 m0, s81
	v_lshl_add_u64 v[20:21], s[62:63], 0, v[172:173]
	global_load_lds_dwordx4 v[18:19], off
	v_lshl_add_u64 v[18:19], s[10:11], 0, v[166:167]
	s_mov_b32 m0, s82
	s_nop 0
	global_load_lds_dwordx4 v[18:19], off
	v_lshl_add_u64 v[18:19], s[62:63], 0, v[168:169]
	s_mov_b32 m0, s6
	s_nop 0
	global_load_lds_dwordx4 v[18:19], off
	s_mov_b32 m0, s84
	s_nop 0
	global_load_lds_dwordx4 v[20:21], off
	s_waitcnt vmcnt(8)
	s_waitcnt lgkmcnt(0)
	s_barrier
	s_setprio 1
	s_waitcnt lgkmcnt(0)
	v_mfma_f32_16x16x128_f8f6f4 v[106:109], v[6:13], v[194:201], v[106:109]
	v_mfma_f32_16x16x128_f8f6f4 v[102:105], v[22:29], v[194:201], v[102:105]
	v_mfma_f32_16x16x128_f8f6f4 v[82:85], v[6:13], v[212:219], v[82:85]
	v_mfma_f32_16x16x128_f8f6f4 v[78:81], v[22:29], v[212:219], v[78:81]
	v_mfma_f32_16x16x128_f8f6f4 v[66:69], v[6:13], v[226:233], v[66:69]
	v_mfma_f32_16x16x128_f8f6f4 v[62:65], v[22:29], v[226:233], v[62:65]
	v_mfma_f32_16x16x128_f8f6f4 v[50:53], v[6:13], v[236:243], v[50:53]
	v_mfma_f32_16x16x128_f8f6f4 v[46:49], v[22:29], v[236:243], v[46:49]
	s_setprio 0
	s_setprio 1
	v_mfma_f32_16x16x128_f8f6f4 v[94:97], v[30:37], v[194:201], v[94:97]
	v_mfma_f32_16x16x128_f8f6f4 v[86:89], v[180:187], v[194:201], v[86:89]
	v_mfma_f32_16x16x128_f8f6f4 v[74:77], v[30:37], v[212:219], v[74:77]
	v_mfma_f32_16x16x128_f8f6f4 v[70:73], v[180:187], v[212:219], v[70:73]
	v_mfma_f32_16x16x128_f8f6f4 v[58:61], v[30:37], v[226:233], v[58:61]
	v_mfma_f32_16x16x128_f8f6f4 v[54:57], v[180:187], v[226:233], v[54:57]
	v_mfma_f32_16x16x128_f8f6f4 v[42:45], v[30:37], v[236:243], v[42:45]
	v_mfma_f32_16x16x128_f8f6f4 v[38:41], v[180:187], v[236:243], v[38:41]
	s_setprio 0
	s_barrier
; #define PG8_STAGE(bufoff, gbase, voff) do { _Pragma("unroll") for (int _i = 0; _i < 2; ++_i) \
;         __builtin_amdgcn_global_load_lds((const unsigned*)((const char*)(gbase) + (voff)[_i]), (LAS unsigned*)(lds + (bufoff) + ldsw + _i * 8192), 16, 0, 0); } while (0)
; #define PG8_LDA(dst, b, h) do { if constexpr (F8) { _Pragma("unroll") for (int m = 0; m < 4; ++m) dst##8[m] = PG8_LD8(lds + PG8_SA(b, h) + aoff + m * 2048); } else { \
;         _Pragma("unroll") for (int m = 0; m < 4; ++m) _Pragma("unroll") for (int k = 0; k < 2; ++k) dst[m][k] = *(const LAS bf16x8*)(lds + PG8_SA(b, h) + aoff + m * 2048 + k * 1024); } } while (0)
; #define PG8_LDB(dst, b, h) do { if constexpr (F8) { _Pragma("unroll") for (int n = 0; n < 2; ++n) dst##8[n] = PG8_LD8(lds + PG8_SB(b, h) + boff + n * 2048); } else { \
;         _Pragma("unroll") for (int n = 0; n < 2; ++n) _Pragma("unroll") for (int k = 0; k < 2; ++k) dst[n][k] = *(const LAS bf16x8*)(lds + PG8_SB(b, h) + boff + n * 2048 + k * 1024); } } while (0)
; #define PG8_WAIT_V(n) asm volatile("s_waitcnt vmcnt(" #n ")" ::: "memory")
; #define PG8_WAIT_L(n) asm volatile("s_waitcnt lgkmcnt(" #n ")" ::: "memory")
; #define PG8_BAR __builtin_amdgcn_s_barrier()
; #define PG8_SCHED __builtin_amdgcn_sched_barrier(0)
; template <class Epi, class Sched, bool F8 = false>
; DI void gemm_phase(LAS unsigned char* lds, const int K, const Sched& S, const Epi& E) {
;     ...
;             PG8_LDB(B0, 1, 0); PG8_LDB(B1, 1, 1); PG8_SCHED; PG8_LDA(At, 1, 0); PG8_STAGE(PG8_SA(0, 1), a2, oA[1]);
;             PG8_WAIT_V(8); PG8_WAIT_L(0); PG8_BAR; PG8_MMA(0, 0, At, B0); PG8_MMA(0, 1, At, B1); PG8_BAR; PG8_SCHED;
;             PG8_LDA(At, 1, 1); PG8_STAGE(PG8_SB(1, 0), b3, voffB); PG8_STAGE(PG8_SB(1, 1), b3 + hstep, voffB); PG8_STAGE(PG8_SA(1, 0), a3, oA[0]);
;             PG8_WAIT_V(8); PG8_WAIT_L(0); PG8_BAR; PG8_MMA(1, 0, At, B0); PG8_MMA(1, 1, At, B1); PG8_BAR; PG8_SCHED;
	ds_read_b128 v[22:25], v192
	ds_read_b128 v[26:29], v192 offset:1024
	ds_read_b128 v[30:33], v192 offset:2048
	ds_read_b128 v[34:37], v192 offset:3072
	ds_read_b128 v[6:9], v193
	ds_read_b128 v[10:13], v193 offset:1024
	ds_read_b128 v[180:183], v193 offset:2048
	ds_read_b128 v[184:187], v193 offset:3072
	s_mov_b32 m0, s85
	v_lshl_add_u64 v[220:221], s[62:63], 0, v[170:171]
	ds_read_b128 v[194:197], v189 offset:32768
	ds_read_b128 v[198:201], v189 offset:33792
	ds_read_b128 v[212:215], v189 offset:34816
	ds_read_b128 v[216:219], v189 offset:35840
	ds_read_b128 v[226:229], v189 offset:36864
	ds_read_b128 v[230:233], v189 offset:37888
	ds_read_b128 v[236:239], v189 offset:38912
	ds_read_b128 v[240:243], v189 offset:39936
	global_load_lds_dwordx4 v[220:221], off
	v_lshl_add_u64 v[220:221], s[62:63], 0, v[174:175]
	s_mov_b32 m0, s86
	s_nop 0
	global_load_lds_dwordx4 v[220:221], off
	s_waitcnt vmcnt(8)
	s_waitcnt lgkmcnt(0)
	s_barrier
	s_setprio 1
	s_waitcnt lgkmcnt(0)
	v_mfma_f32_16x16x128_f8f6f4 v[162:165], v[22:29], v[194:201], v[162:165]
	v_mfma_f32_16x16x128_f8f6f4 v[158:161], v[30:37], v[194:201], v[158:161]
	v_mfma_f32_16x16x128_f8f6f4 v[146:149], v[22:29], v[212:219], v[146:149]
	v_mfma_f32_16x16x128_f8f6f4 v[142:145], v[30:37], v[212:219], v[142:145]
	v_mfma_f32_16x16x128_f8f6f4 v[130:133], v[22:29], v[226:233], v[130:133]
	v_mfma_f32_16x16x128_f8f6f4 v[126:129], v[30:37], v[226:233], v[126:129]
	v_mfma_f32_16x16x128_f8f6f4 v[114:117], v[22:29], v[236:243], v[114:117]
	v_mfma_f32_16x16x128_f8f6f4 v[110:113], v[30:37], v[236:243], v[110:113]
	s_setprio 0
	s_setprio 1
	v_mfma_f32_16x16x128_f8f6f4 v[154:157], v[6:13], v[194:201], v[154:157]
	v_mfma_f32_16x16x128_f8f6f4 v[150:153], v[180:187], v[194:201], v[150:153]
	v_mfma_f32_16x16x128_f8f6f4 v[138:141], v[6:13], v[212:219], v[138:141]
	v_mfma_f32_16x16x128_f8f6f4 v[134:137], v[180:187], v[212:219], v[134:137]
	v_mfma_f32_16x16x128_f8f6f4 v[122:125], v[6:13], v[226:233], v[122:125]
	v_mfma_f32_16x16x128_f8f6f4 v[118:121], v[180:187], v[226:233], v[118:121]
	v_mfma_f32_16x16x128_f8f6f4 v[98:101], v[6:13], v[236:243], v[98:101]
	v_mfma_f32_16x16x128_f8f6f4 v[90:93], v[180:187], v[236:243], v[90:93]
	s_setprio 0
	s_barrier
	s_mov_b32 m0, s90
	v_lshl_add_u64 v[14:15], v[14:15], 0, s[24:25]
	s_add_u32 s10, s60, 0x20080
	ds_read_b128 v[194:197], v189 offset:49152
	ds_read_b128 v[198:201], v189 offset:50176
	ds_read_b128 v[212:215], v189 offset:51200
	ds_read_b128 v[216:219], v189 offset:52224
	ds_read_b128 v[226:229], v189 offset:53248
	ds_read_b128 v[230:233], v189 offset:54272
	ds_read_b128 v[236:239], v189 offset:55296
	ds_read_b128 v[240:243], v189 offset:56320
	global_load_lds_dwordx4 v[14:15], off
	v_lshl_add_u64 v[14:15], v[16:17], 0, s[24:25]
	s_mov_b32 m0, s91
	s_addc_u32 s11, s61, 0
	global_load_lds_dwordx4 v[14:15], off
	v_lshl_add_u64 v[14:15], s[10:11], 0, v[2:3]
	s_mov_b32 m0, s95
	s_nop 0
	global_load_lds_dwordx4 v[14:15], off
	v_lshl_add_u64 v[14:15], s[10:11], 0, v[166:167]
	s_mov_b32 m0, s96
	s_nop 0
	global_load_lds_dwordx4 v[14:15], off
	v_lshl_add_u64 v[14:15], v[18:19], 0, s[24:25]
	s_mov_b32 m0, s92
	s_nop 0
	global_load_lds_dwordx4 v[14:15], off
	v_lshl_add_u64 v[14:15], v[20:21], 0, s[24:25]
	s_mov_b32 m0, s93
	s_nop 0
	global_load_lds_dwordx4 v[14:15], off
	s_waitcnt vmcnt(8)
	s_waitcnt lgkmcnt(0)
	s_barrier
	s_setprio 1
	s_waitcnt lgkmcnt(0)
	v_mfma_f32_16x16x128_f8f6f4 v[106:109], v[22:29], v[194:201], v[106:109]
	v_mfma_f32_16x16x128_f8f6f4 v[102:105], v[30:37], v[194:201], v[102:105]
	v_mfma_f32_16x16x128_f8f6f4 v[82:85], v[22:29], v[212:219], v[82:85]
	v_mfma_f32_16x16x128_f8f6f4 v[78:81], v[30:37], v[212:219], v[78:81]
	v_mfma_f32_16x16x128_f8f6f4 v[66:69], v[22:29], v[226:233], v[66:69]
	v_mfma_f32_16x16x128_f8f6f4 v[62:65], v[30:37], v[226:233], v[62:65]
	v_mfma_f32_16x16x128_f8f6f4 v[50:53], v[22:29], v[236:243], v[50:53]
	v_mfma_f32_16x16x128_f8f6f4 v[46:49], v[30:37], v[236:243], v[46:49]
	s_setprio 0
	s_setprio 1
	v_mfma_f32_16x16x128_f8f6f4 v[94:97], v[6:13], v[194:201], v[94:97]
	v_mfma_f32_16x16x128_f8f6f4 v[86:89], v[180:187], v[194:201], v[86:89]
	v_mfma_f32_16x16x128_f8f6f4 v[74:77], v[6:13], v[212:219], v[74:77]
	v_mfma_f32_16x16x128_f8f6f4 v[70:73], v[180:187], v[212:219], v[70:73]
	v_mfma_f32_16x16x128_f8f6f4 v[58:61], v[6:13], v[226:233], v[58:61]
	v_mfma_f32_16x16x128_f8f6f4 v[54:57], v[180:187], v[226:233], v[54:57]
	v_mfma_f32_16x16x128_f8f6f4 v[42:45], v[6:13], v[236:243], v[42:45]
	v_mfma_f32_16x16x128_f8f6f4 v[38:41], v[180:187], v[236:243], v[38:41]
	s_setprio 0
	s_add_i32 s9, s9, 2
	s_add_u32 s7, s7, 0x100
	s_addc_u32 s8, s8, 0
	s_add_u32 s58, s58, 0x100
	s_addc_u32 s59, s59, 0
	s_cmp_gt_u32 s9, 5
	s_barrier
	s_cbranch_scc0 .LBB0_1043
	s_and_b64 vcc, exec, s[46:47]
	s_cbranch_vccz .LBB0_1046
	s_barrier

; #define PG8_STAGE(bufoff, gbase, voff) do { _Pragma("unroll") for (int _i = 0; _i < 2; ++_i) \
;         __builtin_amdgcn_global_load_lds((const unsigned*)((const char*)(gbase) + (voff)[_i]), (LAS unsigned*)(lds + (bufoff) + ldsw + _i * 8192), 16, 0, 0); } while (0)
; #define PG8_LDA(dst, b, h) do { if constexpr (F8) { _Pragma("unroll") for (int m = 0; m < 4; ++m) dst##8[m] = PG8_LD8(lds + PG8_SA(b, h) + aoff + m * 2048); } else { \
;         _Pragma("unroll") for (int m = 0; m < 4; ++m) _Pragma("unroll") for (int k = 0; k < 2; ++k) dst[m][k] = *(const LAS bf16x8*)(lds + PG8_SA(b, h) + aoff + m * 2048 + k * 1024); } } while (0)
; #define PG8_LDB(dst, b, h) do { if constexpr (F8) { _Pragma("unroll") for (int n = 0; n < 2; ++n) dst##8[n] = PG8_LD8(lds + PG8_SB(b, h) + boff + n * 2048); } else { \
;         _Pragma("unroll") for (int n = 0; n < 2; ++n) _Pragma("unroll") for (int k = 0; k < 2; ++k) dst[n][k] = *(const LAS bf16x8*)(lds + PG8_SB(b, h) + boff + n * 2048 + k * 1024); } } while (0)
; #define PG8_WAIT_L(n) asm volatile("s_waitcnt lgkmcnt(" #n ")" ::: "memory")
; #define PG8_BAR __builtin_amdgcn_s_barrier()
; template <class Epi, class Sched, bool F8 = false>
; DI void gemm_phase(LAS unsigned char* lds, const int K, const Sched& S, const Epi& E) {
;     ...
;             const bool last = (t == nt - 2); const int sxe = (t == 0) ? sx : 0;
;             const char* a1 = cA + (size_t)(t + 1) * kstep;
;             const char* a2 = last ? nA : cA + (size_t)(t + 2) * kstep; const char* b2 = last ? nB : cB + (size_t)(t + 2) * kstep;
;             const char* a3 = a2 + kstep; const char* b3 = b2 + kstep;
;             PG8_LDB(B0, 0, 0); PG8_LDB(B1, 0, 1); PG8_SCHED; PG8_LDA(At, 0, 0); PG8_STAGE(PG8_SA(1, 1), a1, oA[1]);
;             if (last && has_next) S.a_off(nxt, tid, oA);
;             PG8_WAIT_VX(sxe); PG8_WAIT_L(0); PG8_BAR; if (F8 && t == 0) { PG8_MMA0(0, 0, At, B0); PG8_MMA0(0, 1, At, B1); } else { PG8_MMA(0, 0, At, B0); PG8_MMA(0, 1, At, B1); } PG8_BAR; PG8_SCHED;
;             PG8_LDA(At, 0, 1); PG8_STAGE(PG8_SB(0, 0), b2, voffB); PG8_STAGE(PG8_SB(0, 1), b2 + hstep, voffB); PG8_STAGE(PG8_SA(0, 0), a2, oA[0]);
;             PG8_WAIT_VX(sxe); PG8_WAIT_L(0); PG8_BAR; if (F8 && t == 0) { PG8_MMA0(1, 0, At, B0); PG8_MMA0(1, 1, At, B1); } else { PG8_MMA(1, 0, At, B0); PG8_MMA(1, 1, At, B1); } PG8_BAR; PG8_SCHED;
.LBB0_1362:
	s_waitcnt vmcnt(8)
	s_add_u32 s10, s60, 0x80
	s_waitcnt lgkmcnt(0)
	s_addc_u32 s11, s61, 0
	s_and_b64 s[8:9], s[62:63], exec
	v_mov_b32_e32 v217, v4
	v_mov_b32_e32 v221, v4
	s_cselect_b32 vcc_hi, s43, s11
	s_cselect_b32 vcc_lo, s42, s10
	s_cselect_b32 s63, s59, s7
	s_cselect_b32 s62, s58, s6
	s_barrier
	s_setprio 1
	s_waitcnt lgkmcnt(0)
	v_mfma_f32_16x16x128_f8f6f4 v[190:193], v[30:37], v[62:69], v[190:193]
	v_mfma_f32_16x16x128_f8f6f4 v[182:185], v[22:29], v[62:69], v[182:185]
	v_mfma_f32_16x16x128_f8f6f4 v[174:177], v[30:37], v[54:61], v[174:177]
	v_mfma_f32_16x16x128_f8f6f4 v[166:169], v[22:29], v[54:61], v[166:169]
	v_mfma_f32_16x16x128_f8f6f4 v[158:161], v[30:37], v[46:53], v[158:161]
	v_mfma_f32_16x16x128_f8f6f4 v[150:153], v[22:29], v[46:53], v[150:153]
	v_mfma_f32_16x16x128_f8f6f4 v[142:145], v[30:37], v[38:45], v[142:145]
	v_mfma_f32_16x16x128_f8f6f4 v[134:137], v[22:29], v[38:45], v[134:137]
	s_setprio 0
	s_setprio 1
	v_mfma_f32_16x16x128_f8f6f4 v[194:197], v[14:21], v[62:69], v[194:197]
	v_mfma_f32_16x16x128_f8f6f4 v[186:189], v[6:13], v[62:69], v[186:189]
	v_mfma_f32_16x16x128_f8f6f4 v[178:181], v[14:21], v[54:61], v[178:181]
	v_mfma_f32_16x16x128_f8f6f4 v[170:173], v[6:13], v[54:61], v[170:173]
	v_mfma_f32_16x16x128_f8f6f4 v[162:165], v[14:21], v[46:53], v[162:165]
	v_mfma_f32_16x16x128_f8f6f4 v[154:157], v[6:13], v[46:53], v[154:157]
	v_mfma_f32_16x16x128_f8f6f4 v[146:149], v[14:21], v[38:45], v[146:149]
	v_mfma_f32_16x16x128_f8f6f4 v[138:141], v[6:13], v[38:45], v[138:141]
	s_setprio 0
	s_barrier
	s_mov_b32 m0, s0
	v_lshl_add_u64 v[38:39], s[62:63], 0, v[212:213]
	s_add_u32 s8, s62, 0x20000
	ds_read_b128 v[46:49], v240 offset:16384
	ds_read_b128 v[50:53], v240 offset:17408
	ds_read_b128 v[54:57], v240 offset:18432
	ds_read_b128 v[58:61], v240 offset:19456
	ds_read_b128 v[62:65], v240 offset:20480
	ds_read_b128 v[66:69], v240 offset:21504
	ds_read_b128 v[226:229], v240 offset:22528
	ds_read_b128 v[230:233], v240 offset:23552
	global_load_lds_dwordx4 v[38:39], off
	v_lshl_add_u64 v[40:41], s[62:63], 0, v[2:3]
	s_mov_b32 m0, s97
	s_addc_u32 s9, s63, 0
	global_load_lds_dwordx4 v[40:41], off
	v_lshl_add_u64 v[42:43], s[8:9], 0, v[212:213]
	s_mov_b32 m0, s30
	v_mov_b32_e32 v215, v4
	global_load_lds_dwordx4 v[42:43], off
	v_lshl_add_u64 v[42:43], s[8:9], 0, v[2:3]
	s_mov_b32 m0, s31
	v_mov_b32_e32 v219, v4
	global_load_lds_dwordx4 v[42:43], off
	s_mov_b32 m0, s5
	v_lshl_add_u64 v[44:45], vcc, 0, v[214:215]
	global_load_lds_dwordx4 v214, vcc
	s_mov_b32 m0, s95
	v_lshl_add_u64 v[42:43], vcc, 0, v[218:219]
	global_load_lds_dwordx4 v218, vcc
	s_waitcnt vmcnt(8)
	s_waitcnt lgkmcnt(0)
	s_barrier
	s_setprio 1
	s_waitcnt lgkmcnt(0)
	v_mfma_f32_16x16x128_f8f6f4 v[126:129], v[30:37], v[46:53], v[126:129]
	v_mfma_f32_16x16x128_f8f6f4 v[118:121], v[22:29], v[46:53], v[118:121]
	v_mfma_f32_16x16x128_f8f6f4 v[110:113], v[30:37], v[54:61], v[110:113]
	v_mfma_f32_16x16x128_f8f6f4 v[102:105], v[22:29], v[54:61], v[102:105]
	v_mfma_f32_16x16x128_f8f6f4 v[94:97], v[30:37], v[62:69], v[94:97]
	v_mfma_f32_16x16x128_f8f6f4 v[86:89], v[22:29], v[62:69], v[86:89]
	v_mfma_f32_16x16x128_f8f6f4 v[78:81], v[30:37], v[226:233], v[78:81]
	v_mfma_f32_16x16x128_f8f6f4 v[70:73], v[22:29], v[226:233], v[70:73]
	s_setprio 0
	s_setprio 1
	v_mfma_f32_16x16x128_f8f6f4 v[130:133], v[14:21], v[46:53], v[130:133]
	v_mfma_f32_16x16x128_f8f6f4 v[122:125], v[6:13], v[46:53], v[122:125]
	v_mfma_f32_16x16x128_f8f6f4 v[114:117], v[14:21], v[54:61], v[114:117]
	v_mfma_f32_16x16x128_f8f6f4 v[106:109], v[6:13], v[54:61], v[106:109]
	v_mfma_f32_16x16x128_f8f6f4 v[98:101], v[14:21], v[62:69], v[98:101]
	v_mfma_f32_16x16x128_f8f6f4 v[90:93], v[6:13], v[62:69], v[90:93]
	v_mfma_f32_16x16x128_f8f6f4 v[82:85], v[14:21], v[226:233], v[82:85]
	v_mfma_f32_16x16x128_f8f6f4 v[74:77], v[6:13], v[226:233], v[74:77]
	s_setprio 0
	s_barrier
; #define PG8_STAGE(bufoff, gbase, voff) do { _Pragma("unroll") for (int _i = 0; _i < 2; ++_i) \
;         __builtin_amdgcn_global_load_lds((const unsigned*)((const char*)(gbase) + (voff)[_i]), (LAS unsigned*)(lds + (bufoff) + ldsw + _i * 8192), 16, 0, 0); } while (0)
; #define PG8_LDA(dst, b, h) do { if constexpr (F8) { _Pragma("unroll") for (int m = 0; m < 4; ++m) dst##8[m] = PG8_LD8(lds + PG8_SA(b, h) + aoff + m * 2048); } else { \
;         _Pragma("unroll") for (int m = 0; m < 4; ++m) _Pragma("unroll") for (int k = 0; k < 2; ++k) dst[m][k] = *(const LAS bf16x8*)(lds + PG8_SA(b, h) + aoff + m * 2048 + k * 1024); } } while (0)
; #define PG8_LDB(dst, b, h) do { if constexpr (F8) { _Pragma("unroll") for (int n = 0; n < 2; ++n) dst##8[n] = PG8_LD8(lds + PG8_SB(b, h) + boff + n * 2048); } else { \
;         _Pragma("unroll") for (int n = 0; n < 2; ++n) _Pragma("unroll") for (int k = 0; k < 2; ++k) dst[n][k] = *(const LAS bf16x8*)(lds + PG8_SB(b, h) + boff + n * 2048 + k * 1024); } } while (0)
; #define PG8_WAIT_V(n) asm volatile("s_waitcnt vmcnt(" #n ")" ::: "memory")
; #define PG8_WAIT_L(n) asm volatile("s_waitcnt lgkmcnt(" #n ")" ::: "memory")
; #define PG8_BAR __builtin_amdgcn_s_barrier()
; #define PG8_SCHED __builtin_amdgcn_sched_barrier(0)
; template <class Epi, class Sched, bool F8 = false>
; DI void gemm_phase(LAS unsigned char* lds, const int K, const Sched& S, const Epi& E) {
;     ...
;             PG8_LDB(B0, 1, 0); PG8_LDB(B1, 1, 1); PG8_SCHED; PG8_LDA(At, 1, 0); PG8_STAGE(PG8_SA(0, 1), a2, oA[1]);
;             PG8_WAIT_V(8); PG8_WAIT_L(0); PG8_BAR; PG8_MMA(0, 0, At, B0); PG8_MMA(0, 1, At, B1); PG8_BAR; PG8_SCHED;
;             PG8_LDA(At, 1, 1); PG8_STAGE(PG8_SB(1, 0), b3, voffB); PG8_STAGE(PG8_SB(1, 1), b3 + hstep, voffB); PG8_STAGE(PG8_SA(1, 0), a3, oA[0]);
;             PG8_WAIT_V(8); PG8_WAIT_L(0); PG8_BAR; PG8_MMA(1, 0, At, B0); PG8_MMA(1, 1, At, B1); PG8_BAR; PG8_SCHED;
	ds_read_b128 v[14:17], v242
	ds_read_b128 v[18:21], v242 offset:1024
	ds_read_b128 v[22:25], v242 offset:2048
	ds_read_b128 v[26:29], v242 offset:3072
	ds_read_b128 v[6:9], v243
	ds_read_b128 v[10:13], v243 offset:1024
	ds_read_b128 v[30:33], v243 offset:2048
	ds_read_b128 v[34:37], v243 offset:3072
	s_mov_b32 m0, s44
	v_lshl_add_u64 v[198:199], vcc, 0, v[216:217]
	ds_read_b128 v[46:49], v240 offset:32768
	ds_read_b128 v[50:53], v240 offset:33792
	ds_read_b128 v[54:57], v240 offset:34816
	ds_read_b128 v[58:61], v240 offset:35840
	ds_read_b128 v[62:65], v240 offset:36864
	ds_read_b128 v[66:69], v240 offset:37888
	ds_read_b128 v[226:229], v240 offset:38912
	ds_read_b128 v[230:233], v240 offset:39936
	global_load_lds_dwordx4 v[198:199], off
	v_lshl_add_u64 v[198:199], vcc, 0, v[220:221]
	s_mov_b32 m0, s45
	s_nop 0
	global_load_lds_dwordx4 v[198:199], off
	s_waitcnt vmcnt(8)
	s_waitcnt lgkmcnt(0)
	s_barrier
	s_setprio 1
	s_waitcnt lgkmcnt(0)
	v_mfma_f32_16x16x128_f8f6f4 v[190:193], v[14:21], v[46:53], v[190:193]
	v_mfma_f32_16x16x128_f8f6f4 v[182:185], v[22:29], v[46:53], v[182:185]
	v_mfma_f32_16x16x128_f8f6f4 v[174:177], v[14:21], v[54:61], v[174:177]
	v_mfma_f32_16x16x128_f8f6f4 v[166:169], v[22:29], v[54:61], v[166:169]
	v_mfma_f32_16x16x128_f8f6f4 v[158:161], v[14:21], v[62:69], v[158:161]
	v_mfma_f32_16x16x128_f8f6f4 v[150:153], v[22:29], v[62:69], v[150:153]
	v_mfma_f32_16x16x128_f8f6f4 v[142:145], v[14:21], v[226:233], v[142:145]
	v_mfma_f32_16x16x128_f8f6f4 v[134:137], v[22:29], v[226:233], v[134:137]
	s_setprio 0
	s_setprio 1
	v_mfma_f32_16x16x128_f8f6f4 v[194:197], v[6:13], v[46:53], v[194:197]
	v_mfma_f32_16x16x128_f8f6f4 v[186:189], v[30:37], v[46:53], v[186:189]
	v_mfma_f32_16x16x128_f8f6f4 v[178:181], v[6:13], v[54:61], v[178:181]
	v_mfma_f32_16x16x128_f8f6f4 v[170:173], v[30:37], v[54:61], v[170:173]
	v_mfma_f32_16x16x128_f8f6f4 v[162:165], v[6:13], v[62:69], v[162:165]
	v_mfma_f32_16x16x128_f8f6f4 v[154:157], v[30:37], v[62:69], v[154:157]
	v_mfma_f32_16x16x128_f8f6f4 v[146:149], v[6:13], v[226:233], v[146:149]
	v_mfma_f32_16x16x128_f8f6f4 v[138:141], v[30:37], v[226:233], v[138:141]
	s_setprio 0
	s_barrier
	s_mov_b32 m0, s83
	v_lshl_add_u64 v[38:39], v[38:39], 0, s[24:25]
	s_add_u32 s8, s62, 0x20080
	ds_read_b128 v[46:49], v240 offset:49152
	ds_read_b128 v[50:53], v240 offset:50176
	ds_read_b128 v[54:57], v240 offset:51200
	ds_read_b128 v[58:61], v240 offset:52224
	ds_read_b128 v[62:65], v240 offset:53248
	ds_read_b128 v[66:69], v240 offset:54272
	ds_read_b128 v[226:229], v240 offset:55296
	ds_read_b128 v[230:233], v240 offset:56320
	global_load_lds_dwordx4 v[38:39], off
	v_lshl_add_u64 v[38:39], v[40:41], 0, s[24:25]
	s_mov_b32 m0, s82
	s_addc_u32 s9, s63, 0
	global_load_lds_dwordx4 v[38:39], off
	v_lshl_add_u64 v[38:39], s[8:9], 0, v[212:213]
	s_mov_b32 m0, s88
	s_nop 0
	global_load_lds_dwordx4 v[38:39], off
	v_lshl_add_u64 v[38:39], s[8:9], 0, v[2:3]
	s_mov_b32 m0, s87
	s_nop 0
	global_load_lds_dwordx4 v[38:39], off
	v_lshl_add_u64 v[38:39], v[44:45], 0, s[24:25]
	s_mov_b32 m0, s84
	s_nop 0
	global_load_lds_dwordx4 v[38:39], off
	v_lshl_add_u64 v[38:39], v[42:43], 0, s[24:25]
	s_mov_b32 m0, s85
	s_nop 0
	global_load_lds_dwordx4 v[38:39], off
	s_waitcnt vmcnt(8)
	s_waitcnt lgkmcnt(0)
	s_barrier
	s_setprio 1
	s_waitcnt lgkmcnt(0)
	v_mfma_f32_16x16x128_f8f6f4 v[126:129], v[14:21], v[46:53], v[126:129]
	v_mfma_f32_16x16x128_f8f6f4 v[118:121], v[22:29], v[46:53], v[118:121]
	v_mfma_f32_16x16x128_f8f6f4 v[110:113], v[14:21], v[54:61], v[110:113]
	v_mfma_f32_16x16x128_f8f6f4 v[102:105], v[22:29], v[54:61], v[102:105]
	v_mfma_f32_16x16x128_f8f6f4 v[94:97], v[14:21], v[62:69], v[94:97]
	v_mfma_f32_16x16x128_f8f6f4 v[86:89], v[22:29], v[62:69], v[86:89]
	v_mfma_f32_16x16x128_f8f6f4 v[78:81], v[14:21], v[226:233], v[78:81]
	v_mfma_f32_16x16x128_f8f6f4 v[70:73], v[22:29], v[226:233], v[70:73]
	s_setprio 0
	s_setprio 1
	v_mfma_f32_16x16x128_f8f6f4 v[130:133], v[6:13], v[46:53], v[130:133]
	v_mfma_f32_16x16x128_f8f6f4 v[122:125], v[30:37], v[46:53], v[122:125]
	v_mfma_f32_16x16x128_f8f6f4 v[114:117], v[6:13], v[54:61], v[114:117]
	v_mfma_f32_16x16x128_f8f6f4 v[106:109], v[30:37], v[54:61], v[106:109]
	v_mfma_f32_16x16x128_f8f6f4 v[98:101], v[6:13], v[62:69], v[98:101]
	v_mfma_f32_16x16x128_f8f6f4 v[90:93], v[30:37], v[62:69], v[90:93]
	v_mfma_f32_16x16x128_f8f6f4 v[82:85], v[6:13], v[226:233], v[82:85]
	v_mfma_f32_16x16x128_f8f6f4 v[74:77], v[30:37], v[226:233], v[74:77]
	s_setprio 0
	s_add_i32 s67, s67, 2
	s_add_u32 s6, s6, 0x100
	s_addc_u32 s7, s7, 0
	s_add_u32 s60, s60, 0x100
	s_addc_u32 s61, s61, 0
	s_cmp_gt_u32 s67, 5
	s_barrier
	s_cbranch_scc1 .LBB0_1365

; #define PG8_STAGE(bufoff, gbase, voff) do { _Pragma("unroll") for (int _i = 0; _i < 2; ++_i) \
;         __builtin_amdgcn_global_load_lds((const unsigned*)((const char*)(gbase) + (voff)[_i]), (LAS unsigned*)(lds + (bufoff) + ldsw + _i * 8192), 16, 0, 0); } while (0)
; #define PG8_LDA(dst, b, h) do { if constexpr (F8) { _Pragma("unroll") for (int m = 0; m < 4; ++m) dst##8[m] = PG8_LD8(lds + PG8_SA(b, h) + aoff + m * 2048); } else { \
;         _Pragma("unroll") for (int m = 0; m < 4; ++m) _Pragma("unroll") for (int k = 0; k < 2; ++k) dst[m][k] = *(const LAS bf16x8*)(lds + PG8_SA(b, h) + aoff + m * 2048 + k * 1024); } } while (0)
; #define PG8_LDB(dst, b, h) do { if constexpr (F8) { _Pragma("unroll") for (int n = 0; n < 2; ++n) dst##8[n] = PG8_LD8(lds + PG8_SB(b, h) + boff + n * 2048); } else { \
;         _Pragma("unroll") for (int n = 0; n < 2; ++n) _Pragma("unroll") for (int k = 0; k < 2; ++k) dst[n][k] = *(const LAS bf16x8*)(lds + PG8_SB(b, h) + boff + n * 2048 + k * 1024); } } while (0)
; #define PG8_WAIT_L(n) asm volatile("s_waitcnt lgkmcnt(" #n ")" ::: "memory")
; #define PG8_BAR __builtin_amdgcn_s_barrier()
; template <class Epi, class Sched, bool F8 = false>
; DI void gemm_phase(LAS unsigned char* lds, const int K, const Sched& S, const Epi& E) {
;     ...
;         for (int t = 0; t < nt; t += 2) {
;             const bool last = (t == nt - 2); const int sxe = (t == 0) ? sx : 0;
;             const char* a1 = cA + (size_t)(t + 1) * kstep;
;             const char* a2 = last ? nA : cA + (size_t)(t + 2) * kstep; const char* b2 = last ? nB : cB + (size_t)(t + 2) * kstep;
;             const char* a3 = a2 + kstep; const char* b3 = b2 + kstep;
;             PG8_LDB(B0, 0, 0); PG8_LDB(B1, 0, 1); PG8_SCHED; PG8_LDA(At, 0, 0); PG8_STAGE(PG8_SA(1, 1), a1, oA[1]);
;             if (last && has_next) S.a_off(nxt, tid, oA);
;             PG8_WAIT_VX(sxe); PG8_WAIT_L(0); PG8_BAR; if (F8 && t == 0) { PG8_MMA0(0, 0, At, B0); PG8_MMA0(0, 1, At, B1); } else { PG8_MMA(0, 0, At, B0); PG8_MMA(0, 1, At, B1); } PG8_BAR; PG8_SCHED;
;             PG8_LDA(At, 0, 1); PG8_STAGE(PG8_SB(0, 0), b2, voffB); PG8_STAGE(PG8_SB(0, 1), b2 + hstep, voffB); PG8_STAGE(PG8_SA(0, 0), a2, oA[0]);
;             PG8_WAIT_VX(sxe); PG8_WAIT_L(0); PG8_BAR; if (F8 && t == 0) { PG8_MMA0(1, 0, At, B0); PG8_MMA0(1, 1, At, B1); } else { PG8_MMA(1, 0, At, B0); PG8_MMA(1, 1, At, B1); } PG8_BAR; PG8_SCHED;
.LBB0_1641:
	ds_read_b128 v[6:9], v188
	ds_read_b128 v[10:13], v188 offset:1024
	ds_read_b128 v[22:25], v188 offset:2048
	ds_read_b128 v[26:29], v188 offset:3072
	ds_read_b128 v[30:33], v189
	ds_read_b128 v[34:37], v189 offset:1024
	ds_read_b128 v[180:183], v189 offset:2048
	ds_read_b128 v[184:187], v189 offset:3072
	s_add_u32 s10, s48, 0x80
	s_addc_u32 s11, s49, 0
	s_cmp_eq_u32 s55, 4
	s_cselect_b64 s[30:31], -1, 0
	s_and_b64 s[8:9], s[30:31], exec
	s_cselect_b32 s53, s17, s11
	s_cselect_b32 s52, s43, s10
	s_cselect_b32 s51, s63, s7
	s_cselect_b32 s50, s62, s6
	s_mov_b32 m0, s45
	ds_read_b128 v[14:17], v179
	ds_read_b128 v[18:21], v179 offset:1024
	ds_read_b128 v[192:195], v179 offset:2048
	ds_read_b128 v[196:199], v179 offset:3072
	ds_read_b128 v[212:215], v179 offset:4096
	ds_read_b128 v[216:219], v179 offset:5120
	ds_read_b128 v[226:229], v179 offset:6144
	ds_read_b128 v[230:233], v179 offset:7168
	global_load_lds_dwordx4 v170, s[48:49]
	s_mov_b32 m0, s54
	s_and_b64 vcc, s[46:47], s[30:31]
	global_load_lds_dwordx4 v174, s[48:49]
	s_waitcnt vmcnt(8)
	s_waitcnt lgkmcnt(0)
	v_cndmask_b32_e32 v174, v174, v178, vcc
	v_cndmask_b32_e32 v170, v170, v176, vcc
	v_mov_b32_e32 v175, v4
	v_mov_b32_e32 v171, v4
	s_barrier
	s_setprio 1
	s_waitcnt lgkmcnt(0)
	v_mfma_f32_16x16x128_f8f6f4 v[162:165], v[6:13], v[14:21], v[162:165]
	v_mfma_f32_16x16x128_f8f6f4 v[158:161], v[22:29], v[14:21], v[158:161]
	v_mfma_f32_16x16x128_f8f6f4 v[146:149], v[6:13], v[192:199], v[146:149]
	v_mfma_f32_16x16x128_f8f6f4 v[142:145], v[22:29], v[192:199], v[142:145]
	v_mfma_f32_16x16x128_f8f6f4 v[130:133], v[6:13], v[212:219], v[130:133]
	v_mfma_f32_16x16x128_f8f6f4 v[126:129], v[22:29], v[212:219], v[126:129]
	v_mfma_f32_16x16x128_f8f6f4 v[106:109], v[6:13], v[226:233], v[106:109]
	v_mfma_f32_16x16x128_f8f6f4 v[98:101], v[22:29], v[226:233], v[98:101]
	s_setprio 0
	s_setprio 1
	v_mfma_f32_16x16x128_f8f6f4 v[154:157], v[30:37], v[14:21], v[154:157]
	v_mfma_f32_16x16x128_f8f6f4 v[150:153], v[180:187], v[14:21], v[150:153]
	v_mfma_f32_16x16x128_f8f6f4 v[138:141], v[30:37], v[192:199], v[138:141]
	v_mfma_f32_16x16x128_f8f6f4 v[134:137], v[180:187], v[192:199], v[134:137]
	v_mfma_f32_16x16x128_f8f6f4 v[122:125], v[30:37], v[212:219], v[122:125]
	v_mfma_f32_16x16x128_f8f6f4 v[118:121], v[180:187], v[212:219], v[118:121]
	v_mfma_f32_16x16x128_f8f6f4 v[90:93], v[30:37], v[226:233], v[90:93]
	v_mfma_f32_16x16x128_f8f6f4 v[86:89], v[180:187], v[226:233], v[86:89]
	s_setprio 0
	s_barrier
	s_mov_b32 m0, s83
	v_lshl_add_u64 v[14:15], s[50:51], 0, v[2:3]
	s_add_u32 s8, s50, 0x20000
	ds_read_b128 v[192:195], v179 offset:16384
	ds_read_b128 v[196:199], v179 offset:17408
	ds_read_b128 v[212:215], v179 offset:18432
	ds_read_b128 v[216:219], v179 offset:19456
	ds_read_b128 v[226:229], v179 offset:20480
	ds_read_b128 v[230:233], v179 offset:21504
	ds_read_b128 v[236:239], v179 offset:22528
	ds_read_b128 v[240:243], v179 offset:23552
	global_load_lds_dwordx4 v[14:15], off
	v_lshl_add_u64 v[16:17], s[50:51], 0, v[166:167]
	s_mov_b32 m0, s84
	s_addc_u32 s9, s51, 0
	global_load_lds_dwordx4 v[16:17], off
	v_lshl_add_u64 v[18:19], s[8:9], 0, v[2:3]
	s_mov_b32 m0, s86
	v_lshl_add_u64 v[20:21], s[52:53], 0, v[172:173]
	global_load_lds_dwordx4 v[18:19], off
	v_lshl_add_u64 v[18:19], s[8:9], 0, v[166:167]
	s_mov_b32 m0, s87
	s_nop 0
	global_load_lds_dwordx4 v[18:19], off
	v_lshl_add_u64 v[18:19], s[52:53], 0, v[168:169]
	s_mov_b32 m0, s88
	s_nop 0
	global_load_lds_dwordx4 v[18:19], off
	s_mov_b32 m0, s89
	s_nop 0
	global_load_lds_dwordx4 v[20:21], off
	s_waitcnt vmcnt(8)
	s_waitcnt lgkmcnt(0)
	s_barrier
	s_setprio 1
	s_waitcnt lgkmcnt(0)
	v_mfma_f32_16x16x128_f8f6f4 v[114:117], v[6:13], v[192:199], v[114:117]
	v_mfma_f32_16x16x128_f8f6f4 v[110:113], v[22:29], v[192:199], v[110:113]
	v_mfma_f32_16x16x128_f8f6f4 v[82:85], v[6:13], v[212:219], v[82:85]
	v_mfma_f32_16x16x128_f8f6f4 v[78:81], v[22:29], v[212:219], v[78:81]
	v_mfma_f32_16x16x128_f8f6f4 v[66:69], v[6:13], v[226:233], v[66:69]
	v_mfma_f32_16x16x128_f8f6f4 v[62:65], v[22:29], v[226:233], v[62:65]
	v_mfma_f32_16x16x128_f8f6f4 v[50:53], v[6:13], v[236:243], v[50:53]
	v_mfma_f32_16x16x128_f8f6f4 v[46:49], v[22:29], v[236:243], v[46:49]
	s_setprio 0
	s_setprio 1
	v_mfma_f32_16x16x128_f8f6f4 v[102:105], v[30:37], v[192:199], v[102:105]
	v_mfma_f32_16x16x128_f8f6f4 v[94:97], v[180:187], v[192:199], v[94:97]
	v_mfma_f32_16x16x128_f8f6f4 v[74:77], v[30:37], v[212:219], v[74:77]
	v_mfma_f32_16x16x128_f8f6f4 v[70:73], v[180:187], v[212:219], v[70:73]
	v_mfma_f32_16x16x128_f8f6f4 v[58:61], v[30:37], v[226:233], v[58:61]
	v_mfma_f32_16x16x128_f8f6f4 v[54:57], v[180:187], v[226:233], v[54:57]
	v_mfma_f32_16x16x128_f8f6f4 v[42:45], v[30:37], v[236:243], v[42:45]
	v_mfma_f32_16x16x128_f8f6f4 v[38:41], v[180:187], v[236:243], v[38:41]
	s_setprio 0
	s_barrier
; #define PG8_STAGE(bufoff, gbase, voff) do { _Pragma("unroll") for (int _i = 0; _i < 2; ++_i) \
;         __builtin_amdgcn_global_load_lds((const unsigned*)((const char*)(gbase) + (voff)[_i]), (LAS unsigned*)(lds + (bufoff) + ldsw + _i * 8192), 16, 0, 0); } while (0)
; #define PG8_LDA(dst, b, h) do { if constexpr (F8) { _Pragma("unroll") for (int m = 0; m < 4; ++m) dst##8[m] = PG8_LD8(lds + PG8_SA(b, h) + aoff + m * 2048); } else { \
;         _Pragma("unroll") for (int m = 0; m < 4; ++m) _Pragma("unroll") for (int k = 0; k < 2; ++k) dst[m][k] = *(const LAS bf16x8*)(lds + PG8_SA(b, h) + aoff + m * 2048 + k * 1024); } } while (0)
; #define PG8_LDB(dst, b, h) do { if constexpr (F8) { _Pragma("unroll") for (int n = 0; n < 2; ++n) dst##8[n] = PG8_LD8(lds + PG8_SB(b, h) + boff + n * 2048); } else { \
;         _Pragma("unroll") for (int n = 0; n < 2; ++n) _Pragma("unroll") for (int k = 0; k < 2; ++k) dst[n][k] = *(const LAS bf16x8*)(lds + PG8_SB(b, h) + boff + n * 2048 + k * 1024); } } while (0)
; #define PG8_WAIT_V(n) asm volatile("s_waitcnt vmcnt(" #n ")" ::: "memory")
; #define PG8_WAIT_L(n) asm volatile("s_waitcnt lgkmcnt(" #n ")" ::: "memory")
; #define PG8_BAR __builtin_amdgcn_s_barrier()
; #define PG8_SCHED __builtin_amdgcn_sched_barrier(0)
; template <class Epi, class Sched, bool F8 = false>
; DI void gemm_phase(LAS unsigned char* lds, const int K, const Sched& S, const Epi& E) {
;     ...
;             PG8_LDB(B0, 1, 0); PG8_LDB(B1, 1, 1); PG8_SCHED; PG8_LDA(At, 1, 0); PG8_STAGE(PG8_SA(0, 1), a2, oA[1]);
;             PG8_WAIT_V(8); PG8_WAIT_L(0); PG8_BAR; PG8_MMA(0, 0, At, B0); PG8_MMA(0, 1, At, B1); PG8_BAR; PG8_SCHED;
;             PG8_LDA(At, 1, 1); PG8_STAGE(PG8_SB(1, 0), b3, voffB); PG8_STAGE(PG8_SB(1, 1), b3 + hstep, voffB); PG8_STAGE(PG8_SA(1, 0), a3, oA[0]);
;             PG8_WAIT_V(8); PG8_WAIT_L(0); PG8_BAR; PG8_MMA(1, 0, At, B0); PG8_MMA(1, 1, At, B1); PG8_BAR; PG8_SCHED;
	ds_read_b128 v[22:25], v190
	ds_read_b128 v[26:29], v190 offset:1024
	ds_read_b128 v[30:33], v190 offset:2048
	ds_read_b128 v[34:37], v190 offset:3072
	ds_read_b128 v[6:9], v191
	ds_read_b128 v[10:13], v191 offset:1024
	ds_read_b128 v[180:183], v191 offset:2048
	ds_read_b128 v[184:187], v191 offset:3072
	s_mov_b32 m0, s90
	v_lshl_add_u64 v[200:201], s[52:53], 0, v[170:171]
	ds_read_b128 v[192:195], v179 offset:32768
	ds_read_b128 v[196:199], v179 offset:33792
	ds_read_b128 v[212:215], v179 offset:34816
	ds_read_b128 v[216:219], v179 offset:35840
	ds_read_b128 v[226:229], v179 offset:36864
	ds_read_b128 v[230:233], v179 offset:37888
	ds_read_b128 v[236:239], v179 offset:38912
	ds_read_b128 v[240:243], v179 offset:39936
	global_load_lds_dwordx4 v[200:201], off
	v_lshl_add_u64 v[200:201], s[52:53], 0, v[174:175]
	s_mov_b32 m0, s91
	s_nop 0
	global_load_lds_dwordx4 v[200:201], off
	s_waitcnt vmcnt(8)
	s_waitcnt lgkmcnt(0)
	s_barrier
	s_setprio 1
	s_waitcnt lgkmcnt(0)
	v_mfma_f32_16x16x128_f8f6f4 v[162:165], v[22:29], v[192:199], v[162:165]
	v_mfma_f32_16x16x128_f8f6f4 v[158:161], v[30:37], v[192:199], v[158:161]
	v_mfma_f32_16x16x128_f8f6f4 v[146:149], v[22:29], v[212:219], v[146:149]
	v_mfma_f32_16x16x128_f8f6f4 v[142:145], v[30:37], v[212:219], v[142:145]
	v_mfma_f32_16x16x128_f8f6f4 v[130:133], v[22:29], v[226:233], v[130:133]
	v_mfma_f32_16x16x128_f8f6f4 v[126:129], v[30:37], v[226:233], v[126:129]
	v_mfma_f32_16x16x128_f8f6f4 v[106:109], v[22:29], v[236:243], v[106:109]
	v_mfma_f32_16x16x128_f8f6f4 v[98:101], v[30:37], v[236:243], v[98:101]
	s_setprio 0
	s_setprio 1
	v_mfma_f32_16x16x128_f8f6f4 v[154:157], v[6:13], v[192:199], v[154:157]
	v_mfma_f32_16x16x128_f8f6f4 v[150:153], v[180:187], v[192:199], v[150:153]
	v_mfma_f32_16x16x128_f8f6f4 v[138:141], v[6:13], v[212:219], v[138:141]
	v_mfma_f32_16x16x128_f8f6f4 v[134:137], v[180:187], v[212:219], v[134:137]
	v_mfma_f32_16x16x128_f8f6f4 v[122:125], v[6:13], v[226:233], v[122:125]
	v_mfma_f32_16x16x128_f8f6f4 v[118:121], v[180:187], v[226:233], v[118:121]
	v_mfma_f32_16x16x128_f8f6f4 v[90:93], v[6:13], v[236:243], v[90:93]
	v_mfma_f32_16x16x128_f8f6f4 v[86:89], v[180:187], v[236:243], v[86:89]
	s_setprio 0
	s_barrier
	s_mov_b32 m0, s5
	v_lshl_add_u64 v[14:15], v[14:15], 0, s[24:25]
	s_add_u32 s8, s50, 0x20080
	ds_read_b128 v[192:195], v179 offset:49152
	ds_read_b128 v[196:199], v179 offset:50176
	ds_read_b128 v[212:215], v179 offset:51200
	ds_read_b128 v[216:219], v179 offset:52224
	ds_read_b128 v[226:229], v179 offset:53248
	ds_read_b128 v[230:233], v179 offset:54272
	ds_read_b128 v[236:239], v179 offset:55296
	ds_read_b128 v[240:243], v179 offset:56320
	global_load_lds_dwordx4 v[14:15], off
	v_lshl_add_u64 v[14:15], v[16:17], 0, s[24:25]
	s_mov_b32 m0, s97
	s_addc_u32 s9, s51, 0
	global_load_lds_dwordx4 v[14:15], off
	v_lshl_add_u64 v[14:15], s[8:9], 0, v[2:3]
	s_mov_b32 m0, s79
	s_nop 0
	global_load_lds_dwordx4 v[14:15], off
	v_lshl_add_u64 v[14:15], s[8:9], 0, v[166:167]
	s_mov_b32 m0, s78
	s_nop 0
	global_load_lds_dwordx4 v[14:15], off
	v_lshl_add_u64 v[14:15], v[18:19], 0, s[24:25]
	s_mov_b32 m0, s80
	s_nop 0
	global_load_lds_dwordx4 v[14:15], off
	v_lshl_add_u64 v[14:15], v[20:21], 0, s[24:25]
	s_mov_b32 m0, s81
	s_nop 0
	global_load_lds_dwordx4 v[14:15], off
	s_waitcnt vmcnt(8)
	s_waitcnt lgkmcnt(0)
	s_barrier
	s_setprio 1
	s_waitcnt lgkmcnt(0)
	v_mfma_f32_16x16x128_f8f6f4 v[114:117], v[22:29], v[192:199], v[114:117]
	v_mfma_f32_16x16x128_f8f6f4 v[110:113], v[30:37], v[192:199], v[110:113]
	v_mfma_f32_16x16x128_f8f6f4 v[82:85], v[22:29], v[212:219], v[82:85]
	v_mfma_f32_16x16x128_f8f6f4 v[78:81], v[30:37], v[212:219], v[78:81]
	v_mfma_f32_16x16x128_f8f6f4 v[66:69], v[22:29], v[226:233], v[66:69]
	v_mfma_f32_16x16x128_f8f6f4 v[62:65], v[30:37], v[226:233], v[62:65]
	v_mfma_f32_16x16x128_f8f6f4 v[50:53], v[22:29], v[236:243], v[50:53]
	v_mfma_f32_16x16x128_f8f6f4 v[46:49], v[30:37], v[236:243], v[46:49]
	s_setprio 0
	s_setprio 1
	v_mfma_f32_16x16x128_f8f6f4 v[102:105], v[6:13], v[192:199], v[102:105]
	v_mfma_f32_16x16x128_f8f6f4 v[94:97], v[180:187], v[192:199], v[94:97]
	v_mfma_f32_16x16x128_f8f6f4 v[74:77], v[6:13], v[212:219], v[74:77]
	v_mfma_f32_16x16x128_f8f6f4 v[70:73], v[180:187], v[212:219], v[70:73]
	v_mfma_f32_16x16x128_f8f6f4 v[58:61], v[6:13], v[226:233], v[58:61]
	v_mfma_f32_16x16x128_f8f6f4 v[54:57], v[180:187], v[226:233], v[54:57]
	v_mfma_f32_16x16x128_f8f6f4 v[42:45], v[6:13], v[236:243], v[42:45]
	v_mfma_f32_16x16x128_f8f6f4 v[38:41], v[180:187], v[236:243], v[38:41]
	s_setprio 0
	s_add_i32 s55, s55, 2
	s_add_u32 s6, s6, 0x100
	s_addc_u32 s7, s7, 0
	s_add_u32 s48, s48, 0x100
	s_addc_u32 s49, s49, 0
	s_cmp_gt_u32 s55, 5
	s_barrier
	s_cbranch_scc0 .LBB0_1641
	s_and_b64 vcc, exec, s[58:59]
	s_cbranch_vccz .LBB0_1644
	s_barrier
